# v75 + 60 half-exchange reduction steps (two selects + ds_bpermute xor 32/16 + wait + add) replaced by v_permlane32/16_swap + add (router reduce8, thin-pass column sums)
# baseline (speedup 1.0000x reference)
.LBB0_103:
	s_add_i32 s16, s25, s40
	s_ashr_i32 s17, s16, 31
	s_lshl_b64 s[10:11], s[16:17], 12
	s_waitcnt lgkmcnt(0)
	v_lshl_add_u64 v[16:17], v[38:39], 0, s[10:11]
	global_load_dwordx4 v[78:81], v[16:17], off nt
	global_load_dwordx4 v[82:85], v[16:17], off offset:1024 nt
	global_load_dwordx4 v[86:89], v[16:17], off offset:2048 nt
	global_load_dwordx4 v[90:93], v[16:17], off offset:3072 nt
	s_lshl_b64 s[10:11], s[16:17], 10
	v_lshl_add_u64 v[126:127], v[40:41], 0, s[10:11]
	s_add_i32 s18, s16, 1
	s_ashr_i32 s19, s18, 31
	s_lshl_b64 s[20:21], s[18:19], 12
	v_lshl_add_u64 v[24:25], v[38:39], 0, s[20:21]
	ds_read_b128 v[94:97], v70
	ds_read_b128 v[98:101], v70 offset:1024
	ds_read_b128 v[102:105], v70 offset:2048
	ds_read_b128 v[106:109], v70 offset:3072
	ds_read_b128 v[110:113], v70 offset:7168
	ds_read_b128 v[114:117], v70 offset:6144
	ds_read_b128 v[118:121], v70 offset:5120
	ds_read_b128 v[122:125], v70 offset:4096
	v_mov_b32_e32 v45, 0
	v_mov_b32_e32 v77, 0
	v_mov_b32_e32 v144, 0
	v_mov_b32_e32 v145, 0
	s_waitcnt vmcnt(3)
	v_pk_fma_f32 v[16:17], v[78:79], v[78:79], 0 op_sel_hi:[1,1,0]
	s_nop 0
	v_pk_fma_f32 v[16:17], v[80:81], v[80:81], v[16:17]
	s_waitcnt vmcnt(2)
	v_pk_fma_f32 v[16:17], v[82:83], v[82:83], v[16:17]
	s_nop 0
	v_pk_fma_f32 v[16:17], v[84:85], v[84:85], v[16:17]
	s_waitcnt vmcnt(1)
	v_pk_fma_f32 v[16:17], v[86:87], v[86:87], v[16:17]
	s_nop 0
	v_pk_fma_f32 v[16:17], v[88:89], v[88:89], v[16:17]
	s_waitcnt vmcnt(0)
	v_pk_fma_f32 v[16:17], v[90:91], v[90:91], v[16:17]
	s_nop 0
	v_pk_fma_f32 v[16:17], v[92:93], v[92:93], v[16:17]
	s_nop 0
	v_add_f32_e32 v16, v16, v17
	s_waitcnt lgkmcnt(0)
	s_nop 1
	v_add_f32_dpp v16, v16, v16 quad_perm:[1,0,3,2] row_mask:0xf bank_mask:0xf
	s_waitcnt lgkmcnt(0)
	s_nop 1
	v_add_f32_dpp v16, v16, v16 quad_perm:[2,3,0,1] row_mask:0xf bank_mask:0xf
	s_waitcnt lgkmcnt(0)
	s_nop 1
	v_add_f32_dpp v16, v16, v16 row_half_mirror row_mask:0xf bank_mask:0xf
	s_waitcnt lgkmcnt(0)
	s_nop 1
	v_add_f32_dpp v16, v16, v16 row_mirror row_mask:0xf bank_mask:0xf
	s_waitcnt lgkmcnt(0)
	v_mov_b32_e32 v17, v16
	s_nop 1
	v_permlane16_swap_b32_e32 v16, v17
	v_add_f32_e32 v16, v16, v17
	s_waitcnt lgkmcnt(0)
	v_mov_b32_e32 v17, v16
	s_nop 1
	v_permlane32_swap_b32_e32 v16, v17
	v_add_f32_e32 v16, v16, v17
	v_fmamk_f32 v16, v16, 0x3a800000, v35
	v_mul_f32_e32 v17, 0x4f800000, v16
	v_cmp_gt_f32_e32 vcc, s28, v16
	s_nop 1
	v_cndmask_b32_e32 v26, v16, v17, vcc
	v_sqrt_f32_e32 v27, v26
	global_load_dwordx4 v[20:23], v[24:25], off nt
	global_load_dwordx4 v[16:19], v[24:25], off offset:1024 nt
	v_add_u32_e32 v28, -1, v27
	v_add_u32_e32 v29, 1, v27
	v_fma_f32 v30, -v28, v27, v26
	v_fma_f32 v31, -v29, v27, v26
	v_cmp_ge_f32_e64 s[10:11], 0, v30
	s_nop 1
	v_cndmask_b32_e64 v27, v27, v28, s[10:11]
	v_cmp_lt_f32_e64 s[10:11], 0, v31
	s_nop 1
	v_cndmask_b32_e64 v27, v27, v29, s[10:11]
	v_mul_f32_e32 v28, 0x37800000, v27
	v_cndmask_b32_e32 v27, v27, v28, vcc
	v_cmp_class_f32_e32 vcc, v26, v71
	s_nop 1
	v_cndmask_b32_e32 v128, v27, v26, vcc
	global_load_dwordx4 v[28:31], v[24:25], off offset:2048 nt
	s_nop 0
	global_load_dwordx4 v[24:27], v[24:25], off offset:3072 nt
	v_div_scale_f32 v129, s[10:11], v128, v128, 1.0
	v_rcp_f32_e32 v130, v129
	v_div_scale_f32 v131, vcc, 1.0, v128, 1.0
	v_fma_f32 v132, -v129, v130, 1.0
	v_fmac_f32_e32 v130, v132, v130
	v_mul_f32_e32 v132, v131, v130
	v_fma_f32 v133, -v129, v132, v131
	v_fmac_f32_e32 v132, v133, v130
	v_fma_f32 v129, -v129, v132, v131
	v_div_fmas_f32 v129, v129, v130, v132
	v_div_fixup_f32 v128, v129, v128, 1.0
	v_pk_mul_f32 v[78:79], v[78:79], v[128:129] op_sel_hi:[1,0]
	v_pk_mul_f32 v[82:83], v[82:83], v[128:129] op_sel_hi:[1,0]
	v_pk_fma_f32 v[130:131], v[50:51], v[78:79], v[0:1]
	v_pk_mul_f32 v[86:87], v[86:87], v[128:129] op_sel_hi:[1,0]
	v_pk_fma_f32 v[134:135], v[54:55], v[82:83], v[4:5]
	v_mul_f32_e32 v82, 0x41000000, v130
	v_mul_f32_e32 v83, 0x41000000, v131
	v_pk_mul_f32 v[80:81], v[80:81], v[128:129] op_sel_hi:[1,0]
	v_pk_mul_f32 v[90:91], v[90:91], v[128:129] op_sel_hi:[1,0]
	v_pk_fma_f32 v[138:139], v[58:59], v[86:87], v[8:9]
	v_mul_f32_e32 v86, 0x41000000, v134
	v_mul_f32_e32 v87, 0x41000000, v135
	v_med3_f32 v82, v82, s29, v73
	v_med3_f32 v83, v83, s29, v73
	v_pk_mul_f32 v[84:85], v[84:85], v[128:129] op_sel_hi:[1,0]
	v_pk_mul_f32 v[88:89], v[88:89], v[128:129] op_sel_hi:[1,0]
	v_pk_mul_f32 v[92:93], v[92:93], v[128:129] op_sel_hi:[1,0]
	v_pk_fma_f32 v[128:129], v[48:49], v[80:81], v[2:3]
	v_pk_fma_f32 v[142:143], v[62:63], v[90:91], v[12:13]
	v_mul_f32_e32 v90, 0x41000000, v138
	v_mul_f32_e32 v91, 0x41000000, v139
	v_pk_fma_f32 v[80:81], v[130:131], v[122:123], 0 op_sel_hi:[1,1,0]
	v_med3_f32 v86, v86, s29, v73
	v_med3_f32 v87, v87, s29, v73
	v_cvt_pk_fp8_f32 v45, v82, v83
	v_mul_f32_e32 v146, 0x41000000, v142
	v_mul_f32_e32 v147, 0x41000000, v143
	v_pk_fma_f32 v[78:79], v[130:131], v[94:95], 0 op_sel_hi:[1,1,0]
	v_med3_f32 v90, v90, s29, v73
	v_med3_f32 v91, v91, s29, v73
	v_pk_fma_f32 v[80:81], v[128:129], v[124:125], v[80:81]
	v_cvt_pk_fp8_f32 v77, v86, v87
	v_pk_fma_f32 v[132:133], v[52:53], v[84:85], v[6:7]
	v_mul_f32_e32 v84, 0x41000000, v128
	v_mul_f32_e32 v85, 0x41000000, v129
	v_med3_f32 v94, v146, s29, v73
	v_med3_f32 v95, v147, s29, v73
	v_pk_fma_f32 v[78:79], v[128:129], v[96:97], v[78:79]
	v_cvt_pk_fp8_f32 v144, v90, v91
	v_pk_fma_f32 v[80:81], v[134:135], v[118:119], v[80:81]
	v_pk_fma_f32 v[136:137], v[56:57], v[88:89], v[10:11]
	v_mul_f32_e32 v88, 0x41000000, v132
	v_mul_f32_e32 v89, 0x41000000, v133
	v_med3_f32 v84, v84, s29, v73
	v_med3_f32 v85, v85, s29, v73
	v_cvt_pk_fp8_f32 v145, v94, v95
	v_pk_fma_f32 v[78:79], v[134:135], v[98:99], v[78:79]
	v_pk_fma_f32 v[80:81], v[132:133], v[120:121], v[80:81]
	v_pk_fma_f32 v[140:141], v[60:61], v[92:93], v[14:15]
	v_mul_f32_e32 v92, 0x41000000, v136
	v_mul_f32_e32 v93, 0x41000000, v137
	v_med3_f32 v88, v88, s29, v73
	v_med3_f32 v89, v89, s29, v73
	v_pk_fma_f32 v[78:79], v[132:133], v[100:101], v[78:79]
	v_pk_fma_f32 v[80:81], v[138:139], v[114:115], v[80:81]
	v_cvt_pk_fp8_f32 v45, v84, v85 op_sel:[0,0,1]
	v_mul_f32_e32 v148, 0x41000000, v140
	v_mul_f32_e32 v149, 0x41000000, v141
	v_med3_f32 v92, v92, s29, v73
	v_med3_f32 v93, v93, s29, v73
	v_pk_fma_f32 v[78:79], v[138:139], v[102:103], v[78:79]
	v_pk_fma_f32 v[80:81], v[136:137], v[116:117], v[80:81]
	v_cvt_pk_fp8_f32 v77, v88, v89 op_sel:[0,0,1]
	v_med3_f32 v122, v148, s29, v73
	v_med3_f32 v123, v149, s29, v73
	v_pk_fma_f32 v[78:79], v[136:137], v[104:105], v[78:79]
	v_cvt_pk_fp8_f32 v144, v92, v93 op_sel:[0,0,1]
	v_pk_fma_f32 v[80:81], v[142:143], v[110:111], v[80:81]
	v_cvt_pk_fp8_f32 v145, v122, v123 op_sel:[0,0,1]
	v_pk_fma_f32 v[78:79], v[142:143], v[106:107], v[78:79]
	v_pk_fma_f32 v[80:81], v[140:141], v[112:113], v[80:81]
	v_pk_fma_f32 v[78:79], v[140:141], v[108:109], v[78:79]
	global_store_dword v[126:127], v45, off
	global_store_dword v[126:127], v77, off offset:256
	global_store_dword v[126:127], v144, off offset:512
	global_store_dword v[126:127], v145, off offset:768
	v_add_f32_e32 v45, v80, v81
	v_add_f32_e32 v94, v78, v79
	ds_read_b128 v[78:81], v70 offset:8192
	ds_read_b128 v[82:85], v70 offset:9216
	ds_read_b128 v[86:89], v70 offset:10240
	ds_read_b128 v[90:93], v70 offset:11264
	s_waitcnt lgkmcnt(3)
	v_pk_fma_f32 v[78:79], v[130:131], v[78:79], 0 op_sel_hi:[1,1,0]
	s_nop 0
	v_pk_fma_f32 v[78:79], v[128:129], v[80:81], v[78:79]
	s_waitcnt lgkmcnt(2)
	v_pk_fma_f32 v[78:79], v[134:135], v[82:83], v[78:79]
	s_nop 0
	v_pk_fma_f32 v[78:79], v[132:133], v[84:85], v[78:79]
	s_waitcnt lgkmcnt(1)
	v_pk_fma_f32 v[78:79], v[138:139], v[86:87], v[78:79]
	s_nop 0
	v_pk_fma_f32 v[78:79], v[136:137], v[88:89], v[78:79]
	s_waitcnt lgkmcnt(0)
	v_pk_fma_f32 v[86:87], v[142:143], v[90:91], v[78:79]
	ds_read_b128 v[78:81], v70 offset:13312
	ds_read_b128 v[82:85], v70 offset:12288
	v_pk_fma_f32 v[86:87], v[140:141], v[92:93], v[86:87]
	s_waitcnt lgkmcnt(0)
	v_pk_fma_f32 v[82:83], v[130:131], v[82:83], 0 op_sel_hi:[1,1,0]
	v_add_f32_e32 v77, v86, v87
	ds_read_b128 v[86:89], v70 offset:15360
	ds_read_b128 v[90:93], v70 offset:14336
	v_pk_fma_f32 v[82:83], v[128:129], v[84:85], v[82:83]
	s_nop 0
	v_pk_fma_f32 v[78:79], v[134:135], v[78:79], v[82:83]
	s_nop 0
	v_pk_fma_f32 v[78:79], v[132:133], v[80:81], v[78:79]
	s_waitcnt lgkmcnt(0)
	v_pk_fma_f32 v[78:79], v[138:139], v[90:91], v[78:79]
	s_nop 0
	v_pk_fma_f32 v[78:79], v[136:137], v[92:93], v[78:79]
	s_nop 0
	v_pk_fma_f32 v[78:79], v[142:143], v[86:87], v[78:79]
	s_nop 0
	v_pk_fma_f32 v[78:79], v[140:141], v[88:89], v[78:79]
	s_nop 0
	v_add_f32_e32 v95, v78, v79
	ds_read_b128 v[78:81], v70 offset:16384
	ds_read_b128 v[82:85], v70 offset:17408
	ds_read_b128 v[86:89], v70 offset:18432
	ds_read_b128 v[90:93], v70 offset:19456
	s_waitcnt lgkmcnt(3)
	v_pk_fma_f32 v[78:79], v[130:131], v[78:79], 0 op_sel_hi:[1,1,0]
	s_nop 0
	v_pk_fma_f32 v[78:79], v[128:129], v[80:81], v[78:79]
	s_waitcnt lgkmcnt(2)
	v_pk_fma_f32 v[78:79], v[134:135], v[82:83], v[78:79]
	s_nop 0
	v_pk_fma_f32 v[78:79], v[132:133], v[84:85], v[78:79]
	s_waitcnt lgkmcnt(1)
	v_pk_fma_f32 v[78:79], v[138:139], v[86:87], v[78:79]
	s_nop 0
	v_pk_fma_f32 v[78:79], v[136:137], v[88:89], v[78:79]
	s_waitcnt lgkmcnt(0)
	v_pk_fma_f32 v[86:87], v[142:143], v[90:91], v[78:79]
	ds_read_b128 v[78:81], v70 offset:21504
	ds_read_b128 v[82:85], v70 offset:20480
	v_pk_fma_f32 v[86:87], v[140:141], v[92:93], v[86:87]
	s_waitcnt lgkmcnt(0)
	v_pk_fma_f32 v[82:83], v[130:131], v[82:83], 0 op_sel_hi:[1,1,0]
	v_add_f32_e32 v96, v86, v87
	ds_read_b128 v[86:89], v70 offset:23552
	ds_read_b128 v[90:93], v70 offset:22528
	v_pk_fma_f32 v[82:83], v[128:129], v[84:85], v[82:83]
	s_nop 0
	v_pk_fma_f32 v[78:79], v[134:135], v[78:79], v[82:83]
	s_nop 0
	v_pk_fma_f32 v[78:79], v[132:133], v[80:81], v[78:79]
	s_waitcnt lgkmcnt(0)
	v_pk_fma_f32 v[78:79], v[138:139], v[90:91], v[78:79]
	s_nop 0
	v_pk_fma_f32 v[78:79], v[136:137], v[92:93], v[78:79]
	s_nop 0
	v_pk_fma_f32 v[78:79], v[142:143], v[86:87], v[78:79]
	s_nop 0
	v_pk_fma_f32 v[78:79], v[140:141], v[88:89], v[78:79]
	s_nop 0
	v_add_f32_e32 v97, v78, v79
	ds_read_b128 v[78:81], v70 offset:24576
	ds_read_b128 v[82:85], v70 offset:25600
	ds_read_b128 v[86:89], v70 offset:26624
	ds_read_b128 v[90:93], v70 offset:27648
	s_waitcnt lgkmcnt(3)
	v_pk_fma_f32 v[78:79], v[130:131], v[78:79], 0 op_sel_hi:[1,1,0]
	s_nop 0
	v_pk_fma_f32 v[78:79], v[128:129], v[80:81], v[78:79]
	s_waitcnt lgkmcnt(2)
	v_pk_fma_f32 v[78:79], v[134:135], v[82:83], v[78:79]
	s_nop 0
	v_pk_fma_f32 v[78:79], v[132:133], v[84:85], v[78:79]
	s_waitcnt lgkmcnt(1)
	v_pk_fma_f32 v[78:79], v[138:139], v[86:87], v[78:79]
	s_nop 0
	v_pk_fma_f32 v[78:79], v[136:137], v[88:89], v[78:79]
	s_waitcnt lgkmcnt(0)
	v_pk_fma_f32 v[86:87], v[142:143], v[90:91], v[78:79]
	ds_read_b128 v[78:81], v70 offset:29696
	ds_read_b128 v[82:85], v70 offset:28672
	v_pk_fma_f32 v[86:87], v[140:141], v[92:93], v[86:87]
	s_waitcnt lgkmcnt(0)
	v_pk_fma_f32 v[82:83], v[130:131], v[82:83], 0 op_sel_hi:[1,1,0]
	v_add_f32_e32 v98, v86, v87
	ds_read_b128 v[86:89], v70 offset:31744
	ds_read_b128 v[90:93], v70 offset:30720
	v_pk_fma_f32 v[82:83], v[128:129], v[84:85], v[82:83]
	s_nop 0
	v_pk_fma_f32 v[78:79], v[134:135], v[78:79], v[82:83]
	s_nop 0
	v_pk_fma_f32 v[78:79], v[132:133], v[80:81], v[78:79]
	s_waitcnt lgkmcnt(0)
	v_pk_fma_f32 v[78:79], v[138:139], v[90:91], v[78:79]
	s_nop 0
	v_pk_fma_f32 v[78:79], v[136:137], v[92:93], v[78:79]
	s_nop 0
	v_pk_fma_f32 v[78:79], v[142:143], v[86:87], v[78:79]
	s_nop 0
	v_pk_fma_f32 v[78:79], v[140:141], v[88:89], v[78:79]
	s_nop 0
	v_add_f32_e32 v78, v78, v79
	s_waitcnt lgkmcnt(0)
	s_nop 1
	v_permlane32_swap_b32_e32 v94, v96
	v_add_f32_e32 v79, v94, v96
	s_waitcnt lgkmcnt(0)
	s_nop 1
	v_permlane32_swap_b32_e32 v45, v97
	v_add_f32_e32 v45, v45, v97
	s_waitcnt lgkmcnt(0)
	s_nop 1
	v_permlane32_swap_b32_e32 v77, v98
	v_add_f32_e32 v77, v77, v98
	s_waitcnt lgkmcnt(0)
	s_nop 1
	v_permlane32_swap_b32_e32 v95, v78
	v_add_f32_e32 v78, v95, v78
	s_waitcnt lgkmcnt(0)
	s_nop 1
	v_permlane16_swap_b32_e32 v79, v77
	v_add_f32_e32 v77, v79, v77
	s_waitcnt lgkmcnt(0)
	s_nop 1
	v_permlane16_swap_b32_e32 v45, v78
	v_add_f32_e32 v45, v45, v78
	v_cndmask_b32_e64 v78, v77, v45, s[6:7]
	s_nop 1
	v_mov_b32_dpp v78, v78 row_ror:8 row_mask:0xf bank_mask:0xf
	v_cndmask_b32_e64 v45, v45, v77, s[6:7]
	s_waitcnt lgkmcnt(0)
	v_add_f32_e32 v45, v45, v78
	s_nop 1
	v_mov_b32_dpp v77, v45 quad_perm:[3,2,1,0] row_mask:0xf bank_mask:0xf
	s_nop 1
	v_mov_b32_dpp v77, v77 row_half_mirror row_mask:0xf bank_mask:0xf
	s_waitcnt lgkmcnt(0)
	v_add_f32_e32 v45, v45, v77
	s_nop 1
	v_mov_b32_dpp v77, v45 quad_perm:[2,3,0,1] row_mask:0xf bank_mask:0xf
	s_waitcnt lgkmcnt(0)
	v_add_f32_e32 v45, v45, v77
	s_nop 1
	v_mov_b32_dpp v77, v45 quad_perm:[1,0,3,2] row_mask:0xf bank_mask:0xf
	s_and_saveexec_b64 s[10:11], s[8:9]
	s_cbranch_execz .LBB0_105
	global_load_dword v78, v[42:43], off
	s_waitcnt lgkmcnt(0)
	v_add_f32_e32 v45, v45, v77
	s_add_i32 s20, s39, s40
	s_ashr_i32 s21, s20, 31
	s_waitcnt vmcnt(0)
	v_add_f32_e32 v45, v45, v78
	v_mul_f32_e64 v77, |v45|, s30
	v_exp_f32_e32 v77, v77
	v_min_f32_e32 v92, 0, v45
	v_add_f32_e32 v45, 1.0, v77
	v_add_f32_e32 v80, -1.0, v45
	v_frexp_mant_f32_e32 v81, v45
	v_cvt_f64_f32_e32 v[78:79], v45
	v_sub_f32_e32 v82, v80, v45
	v_frexp_exp_i32_f64_e32 v78, v[78:79]
	v_cmp_gt_f32_e32 vcc, s31, v81
	v_sub_f32_e32 v80, v77, v80
	v_add_f32_e32 v79, 1.0, v82
	v_subbrev_co_u32_e32 v78, vcc, 0, v78, vcc
	v_add_f32_e32 v79, v80, v79
	v_sub_u32_e32 v80, 0, v78
	v_ldexp_f32 v45, v45, v80
	v_ldexp_f32 v79, v79, v80
	v_add_f32_e32 v80, -1.0, v45
	v_add_f32_e32 v82, 1.0, v45
	v_add_f32_e32 v81, 1.0, v80
	v_add_f32_e32 v83, -1.0, v82
	v_sub_f32_e32 v81, v45, v81
	v_sub_f32_e32 v45, v45, v83
	v_add_f32_e32 v45, v79, v45
	v_add_f32_e32 v83, v79, v81
	v_add_f32_e32 v79, v82, v45
	v_rcp_f32_e32 v86, v79
	v_add_f32_e32 v81, v80, v83
	v_sub_f32_e32 v82, v79, v82
	v_sub_f32_e32 v45, v45, v82
	v_mul_f32_e32 v88, v81, v86
	v_mul_f32_e32 v82, v79, v88
	v_fma_f32 v84, v88, v79, -v82
	v_sub_f32_e32 v80, v81, v80
	v_fmac_f32_e32 v84, v88, v45
	v_sub_f32_e32 v87, v83, v80
	v_add_f32_e32 v80, v82, v84
	v_sub_f32_e32 v83, v81, v80
	v_mov_b32_e32 v85, v80
	v_pk_add_f32 v[80:81], v[80:81], v[82:83] neg_lo:[0,1] neg_hi:[0,1]
	v_cvt_f32_i32_e32 v78, v78
	v_pk_add_f32 v[80:81], v[80:81], v[84:85] neg_lo:[0,1] neg_hi:[0,1]
	v_cmp_neq_f32_e32 vcc, s34, v77
	v_add_f32_e32 v81, v87, v81
	v_add_f32_e32 v80, v80, v81
	v_add_f32_e32 v81, v83, v80
	v_mul_f32_e32 v85, v86, v81
	v_mul_f32_e32 v82, v79, v85
	v_fma_f32 v84, v85, v79, -v82
	v_sub_f32_e32 v83, v83, v81
	v_fmac_f32_e32 v84, v85, v45
	v_add_f32_e32 v87, v80, v83
	v_add_f32_e32 v89, v88, v85
	v_add_f32_e32 v80, v82, v84
	v_sub_f32_e32 v79, v89, v88
	v_sub_f32_e32 v83, v81, v80
	v_sub_f32_e32 v45, v85, v79
	v_mov_b32_e32 v85, v80
	v_pk_add_f32 v[80:81], v[80:81], v[82:83] neg_lo:[0,1] neg_hi:[0,1]
	s_nop 0
	v_pk_add_f32 v[80:81], v[80:81], v[84:85] neg_lo:[0,1] neg_hi:[0,1]
	s_nop 0
	v_add_f32_e32 v79, v87, v81
	v_add_f32_e32 v79, v80, v79
	v_add_f32_e32 v79, v83, v79
	v_mul_f32_e32 v79, v86, v79
	v_add_f32_e32 v45, v45, v79
	v_add_f32_e32 v79, v89, v45
	v_mul_f32_e32 v80, v79, v79
	v_sub_f32_e32 v82, v79, v89
	v_fmamk_f32 v83, v80, 0x3e9b6dac, v72
	v_ldexp_f32 v81, v79, 1
	v_sub_f32_e32 v82, v45, v82
	v_mul_f32_e32 v79, v79, v80
	v_fmaak_f32 v45, v80, v83, 0x3f2aaada
	v_ldexp_f32 v85, v82, 1
	v_pk_mul_f32 v[82:83], v[78:79], v[44:45]
	s_nop 0
	v_fma_f32 v80, v78, s33, -v82
	v_fmac_f32_e32 v80, 0xb102e308, v78
	v_pk_add_f32 v[78:79], v[82:83], v[80:81]
	v_mov_b32_e32 v84, v82
	v_sub_f32_e32 v45, v79, v81
	v_sub_f32_e32 v45, v83, v45
	v_add_f32_e32 v85, v85, v45
	v_pk_add_f32 v[86:87], v[78:79], v[82:83] neg_lo:[0,1] neg_hi:[0,1]
	v_pk_add_f32 v[82:83], v[78:79], v[84:85]
	v_mov_b32_e32 v81, v78
	v_mov_b32_e32 v87, v83
	v_pk_add_f32 v[90:91], v[80:81], v[86:87] neg_lo:[0,1] neg_hi:[0,1]
	v_pk_add_f32 v[80:81], v[80:81], v[86:87]
	v_mov_b32_e32 v89, v78
	v_pk_add_f32 v[86:87], v[80:81], v[78:79] op_sel:[1,0] op_sel_hi:[0,1] neg_lo:[0,1] neg_hi:[0,1]
	v_mov_b32_e32 v88, v85
	v_mov_b32_e32 v84, v83
	v_mov_b32_e32 v85, v81
	v_pk_mov_b32 v[78:79], v[78:79], v[86:87] op_sel:[1,0]
	v_pk_add_f32 v[82:83], v[82:83], v[86:87] op_sel_hi:[1,0] neg_lo:[0,1] neg_hi:[0,1]
	v_pk_add_f32 v[78:79], v[84:85], v[78:79] neg_lo:[0,1] neg_hi:[0,1]
	v_mov_b32_e32 v82, v90
	v_pk_add_f32 v[78:79], v[88:89], v[78:79] neg_lo:[0,1] neg_hi:[0,1]
	v_mov_b32_e32 v91, v81
	v_pk_add_f32 v[82:83], v[82:83], v[78:79]
	s_nop 0
	v_pk_add_f32 v[84:85], v[82:83], v[82:83] op_sel:[0,1] op_sel_hi:[1,0]
	s_nop 0
	v_pk_add_f32 v[80:81], v[80:81], v[84:85] op_sel:[1,0] op_sel_hi:[0,1]
	v_mov_b32_e32 v83, v80
	v_mov_b32_e32 v79, v84
	v_pk_add_f32 v[84:85], v[82:83], v[90:91] neg_lo:[0,1] neg_hi:[0,1]
	s_nop 0
	v_sub_f32_e32 v45, v82, v84
	v_pk_add_f32 v[78:79], v[78:79], v[84:85] neg_lo:[0,1] neg_hi:[0,1]
	v_sub_f32_e32 v45, v90, v45
	v_add_f32_e32 v45, v78, v45
	v_add_f32_e32 v45, v45, v79
	v_add_f32_e32 v45, v80, v45
	v_cndmask_b32_e32 v45, v74, v45, vcc
	v_cmp_ngt_f32_e32 vcc, -1.0, v77
	v_lshl_add_u64 v[78:79], s[20:21], 2, v[46:47]
	s_nop 0
	v_cndmask_b32_e32 v45, v75, v45, vcc
	v_cmp_neq_f32_e32 vcc, -1.0, v77
	s_nop 1
	v_cndmask_b32_e32 v45, v76, v45, vcc
	v_cmp_lt_f32_e64 vcc, |v77|, s35
	s_nop 1
	v_cndmask_b32_e32 v45, v45, v77, vcc
	v_sub_f32_e32 v45, v92, v45
	global_store_dword v[78:79], v45, off
.LBB0_105:
	s_or_b64 exec, exec, s[10:11]
	s_waitcnt vmcnt(7)
	v_pk_fma_f32 v[78:79], v[20:21], v[20:21], 0 op_sel_hi:[1,1,0]
	v_mov_b32_e32 v88, 0
	v_pk_fma_f32 v[78:79], v[22:23], v[22:23], v[78:79]
	s_lshl_b64 s[18:19], s[18:19], 10
	s_waitcnt vmcnt(6)
	v_pk_fma_f32 v[78:79], v[16:17], v[16:17], v[78:79]
	v_lshl_add_u64 v[82:83], v[40:41], 0, s[18:19]
	v_pk_fma_f32 v[78:79], v[18:19], v[18:19], v[78:79]
	s_waitcnt vmcnt(5)
	v_pk_fma_f32 v[78:79], v[28:29], v[28:29], v[78:79]
	s_nop 0
	v_pk_fma_f32 v[78:79], v[30:31], v[30:31], v[78:79]
	s_waitcnt vmcnt(4)
	v_pk_fma_f32 v[78:79], v[24:25], v[24:25], v[78:79]
	s_nop 0
	v_pk_fma_f32 v[78:79], v[26:27], v[26:27], v[78:79]
	s_nop 0
	v_add_f32_e32 v45, v78, v79
	s_waitcnt lgkmcnt(0)
	s_waitcnt lgkmcnt(0)
	s_nop 1
	v_add_f32_dpp v45, v45, v45 quad_perm:[1,0,3,2] row_mask:0xf bank_mask:0xf
	s_waitcnt lgkmcnt(0)
	s_nop 1
	v_add_f32_dpp v45, v45, v45 quad_perm:[2,3,0,1] row_mask:0xf bank_mask:0xf
	s_waitcnt lgkmcnt(0)
	s_nop 1
	v_add_f32_dpp v45, v45, v45 row_half_mirror row_mask:0xf bank_mask:0xf
	s_waitcnt lgkmcnt(0)
	s_nop 1
	v_add_f32_dpp v45, v45, v45 row_mirror row_mask:0xf bank_mask:0xf
	s_waitcnt lgkmcnt(0)
	v_mov_b32_e32 v77, v45
	s_nop 1
	v_permlane16_swap_b32_e32 v45, v77
	v_add_f32_e32 v45, v45, v77
	s_waitcnt lgkmcnt(0)
	v_mov_b32_e32 v77, v45
	s_nop 1
	v_permlane32_swap_b32_e32 v45, v77
	v_add_f32_e32 v45, v45, v77
	v_fmamk_f32 v45, v45, 0x3a800000, v35
	v_mul_f32_e32 v77, 0x4f800000, v45
	v_cmp_gt_f32_e32 vcc, s28, v45
	s_nop 1
	v_cndmask_b32_e32 v45, v45, v77, vcc
	v_sqrt_f32_e32 v77, v45
	s_nop 0
	v_add_u32_e32 v78, -1, v77
	v_add_u32_e32 v79, 1, v77
	v_fma_f32 v80, -v78, v77, v45
	v_fma_f32 v81, -v79, v77, v45
	v_cmp_ge_f32_e64 s[10:11], 0, v80
	s_nop 1
	v_cndmask_b32_e64 v77, v77, v78, s[10:11]
	v_cmp_lt_f32_e64 s[10:11], 0, v81
	s_nop 1
	v_cndmask_b32_e64 v77, v77, v79, s[10:11]
	v_mul_f32_e32 v78, 0x37800000, v77
	v_cndmask_b32_e32 v77, v77, v78, vcc
	v_cmp_class_f32_e32 vcc, v45, v71
	s_nop 1
	v_cndmask_b32_e32 v45, v77, v45, vcc
	v_div_scale_f32 v77, s[10:11], v45, v45, 1.0
	v_rcp_f32_e32 v78, v77
	v_div_scale_f32 v79, vcc, 1.0, v45, 1.0
	v_fma_f32 v80, -v77, v78, 1.0
	v_fmac_f32_e32 v78, v80, v78
	v_mul_f32_e32 v80, v79, v78
	v_fma_f32 v81, -v77, v80, v79
	v_fmac_f32_e32 v80, v81, v78
	v_fma_f32 v77, -v77, v80, v79
	v_div_fmas_f32 v77, v77, v78, v80
	v_div_fixup_f32 v78, v77, v45, 1.0
	v_pk_mul_f32 v[20:21], v[20:21], v[78:79] op_sel_hi:[1,0]
	v_pk_mul_f32 v[84:85], v[30:31], v[78:79] op_sel_hi:[1,0]
	v_pk_fma_f32 v[30:31], v[50:51], v[20:21], v[0:1]
	v_pk_mul_f32 v[22:23], v[22:23], v[78:79] op_sel_hi:[1,0]
	v_mul_f32_e32 v45, 0x41000000, v30
	v_mul_f32_e32 v77, 0x41000000, v31
	v_med3_f32 v45, v45, s29, v73
	v_med3_f32 v77, v77, s29, v73
	v_cvt_pk_fp8_f32 v88, v45, v77
	v_pk_mul_f32 v[16:17], v[16:17], v[78:79] op_sel_hi:[1,0]
	v_pk_mul_f32 v[18:19], v[18:19], v[78:79] op_sel_hi:[1,0]
	v_pk_mul_f32 v[80:81], v[28:29], v[78:79] op_sel_hi:[1,0]
	v_pk_mul_f32 v[86:87], v[24:25], v[78:79] op_sel_hi:[1,0]
	v_pk_mul_f32 v[78:79], v[26:27], v[78:79] op_sel_hi:[1,0]
	v_pk_fma_f32 v[24:25], v[48:49], v[22:23], v[2:3]
	v_pk_fma_f32 v[28:29], v[54:55], v[16:17], v[4:5]
	v_pk_fma_f32 v[16:17], v[60:61], v[78:79], v[14:15]
	v_mul_f32_e32 v78, 0x41000000, v24
	v_mul_f32_e32 v45, 0x41000000, v25
	v_med3_f32 v77, v78, s29, v73
	v_med3_f32 v45, v45, s29, v73
	v_cvt_pk_fp8_f32 v88, v77, v45 op_sel:[0,0,1]
	v_mul_f32_e32 v45, 0x41000000, v28
	v_mul_f32_e32 v77, 0x41000000, v29
	v_pk_fma_f32 v[20:21], v[52:53], v[18:19], v[6:7]
	v_pk_fma_f32 v[18:19], v[56:57], v[84:85], v[10:11]
	v_med3_f32 v45, v45, s29, v73
	v_med3_f32 v77, v77, s29, v73
	v_mov_b32_e32 v84, 0
	v_cvt_pk_fp8_f32 v84, v45, v77
	v_mul_f32_e32 v78, 0x41000000, v20
	v_mul_f32_e32 v45, 0x41000000, v21
	v_pk_fma_f32 v[26:27], v[58:59], v[80:81], v[8:9]
	v_med3_f32 v77, v78, s29, v73
	v_med3_f32 v45, v45, s29, v73
	v_cvt_pk_fp8_f32 v84, v77, v45 op_sel:[0,0,1]
	v_mul_f32_e32 v45, 0x41000000, v26
	v_mul_f32_e32 v77, 0x41000000, v27
	v_med3_f32 v45, v45, s29, v73
	v_med3_f32 v77, v77, s29, v73
	v_mov_b32_e32 v85, 0
	v_cvt_pk_fp8_f32 v85, v45, v77
	v_mul_f32_e32 v78, 0x41000000, v18
	v_mul_f32_e32 v45, 0x41000000, v19
	v_pk_fma_f32 v[22:23], v[62:63], v[86:87], v[12:13]
	v_med3_f32 v77, v78, s29, v73
	v_med3_f32 v45, v45, s29, v73
	v_cvt_pk_fp8_f32 v85, v77, v45 op_sel:[0,0,1]
	v_mul_f32_e32 v45, 0x41000000, v22
	v_mul_f32_e32 v77, 0x41000000, v23
	v_med3_f32 v45, v45, s29, v73
	v_med3_f32 v77, v77, s29, v73
	v_mov_b32_e32 v86, 0
	v_cvt_pk_fp8_f32 v86, v45, v77
	v_mul_f32_e32 v78, 0x41000000, v16
	v_mul_f32_e32 v45, 0x41000000, v17
	v_med3_f32 v77, v78, s29, v73
	v_med3_f32 v45, v45, s29, v73
	v_cvt_pk_fp8_f32 v86, v77, v45 op_sel:[0,0,1]
	ds_read_b128 v[78:81], v70
	global_store_dword v[82:83], v88, off
	global_store_dword v[82:83], v84, off offset:256
	global_store_dword v[82:83], v85, off offset:512
	global_store_dword v[82:83], v86, off offset:768
	ds_read_b128 v[82:85], v70 offset:1024
	ds_read_b128 v[86:89], v70 offset:2048
	s_waitcnt lgkmcnt(2)
	v_pk_fma_f32 v[78:79], v[30:31], v[78:79], 0 op_sel_hi:[1,1,0]
	s_nop 0
	v_pk_fma_f32 v[90:91], v[24:25], v[80:81], v[78:79]
	ds_read_b128 v[78:81], v70 offset:3072
	s_waitcnt lgkmcnt(2)
	v_pk_fma_f32 v[82:83], v[28:29], v[82:83], v[90:91]
	s_nop 0
	v_pk_fma_f32 v[82:83], v[20:21], v[84:85], v[82:83]
	s_waitcnt lgkmcnt(1)
	v_pk_fma_f32 v[82:83], v[26:27], v[86:87], v[82:83]
	s_nop 0
	v_pk_fma_f32 v[82:83], v[18:19], v[88:89], v[82:83]
	s_waitcnt lgkmcnt(0)
	v_pk_fma_f32 v[78:79], v[22:23], v[78:79], v[82:83]
	ds_read_b128 v[82:85], v70 offset:5120
	ds_read_b128 v[86:89], v70 offset:4096
	v_pk_fma_f32 v[78:79], v[16:17], v[80:81], v[78:79]
	s_waitcnt lgkmcnt(0)
	v_pk_fma_f32 v[86:87], v[30:31], v[86:87], 0 op_sel_hi:[1,1,0]
	v_add_f32_e32 v45, v78, v79
	ds_read_b128 v[78:81], v70 offset:7168
	ds_read_b128 v[90:93], v70 offset:6144
	v_pk_fma_f32 v[86:87], v[24:25], v[88:89], v[86:87]
	s_nop 0
	v_pk_fma_f32 v[82:83], v[28:29], v[82:83], v[86:87]
	s_nop 0
	v_pk_fma_f32 v[82:83], v[20:21], v[84:85], v[82:83]
	s_waitcnt lgkmcnt(0)
	v_pk_fma_f32 v[82:83], v[26:27], v[90:91], v[82:83]
	s_nop 0
	v_pk_fma_f32 v[82:83], v[18:19], v[92:93], v[82:83]
	s_nop 0
	v_pk_fma_f32 v[78:79], v[22:23], v[78:79], v[82:83]
	s_nop 0
	v_pk_fma_f32 v[78:79], v[16:17], v[80:81], v[78:79]
	s_nop 0
	v_add_f32_e32 v77, v78, v79
	ds_read_b128 v[78:81], v70 offset:8192
	ds_read_b128 v[82:85], v70 offset:9216
	ds_read_b128 v[86:89], v70 offset:10240
	ds_read_b128 v[90:93], v70 offset:11264
	s_waitcnt lgkmcnt(3)
	v_pk_fma_f32 v[78:79], v[30:31], v[78:79], 0 op_sel_hi:[1,1,0]
	s_nop 0
	v_pk_fma_f32 v[78:79], v[24:25], v[80:81], v[78:79]
	s_waitcnt lgkmcnt(2)
	v_pk_fma_f32 v[78:79], v[28:29], v[82:83], v[78:79]
	s_nop 0
	v_pk_fma_f32 v[78:79], v[20:21], v[84:85], v[78:79]
	s_waitcnt lgkmcnt(1)
	v_pk_fma_f32 v[78:79], v[26:27], v[86:87], v[78:79]
	s_nop 0
	v_pk_fma_f32 v[78:79], v[18:19], v[88:89], v[78:79]
	s_waitcnt lgkmcnt(0)
	v_pk_fma_f32 v[86:87], v[22:23], v[90:91], v[78:79]
	ds_read_b128 v[78:81], v70 offset:13312
	ds_read_b128 v[82:85], v70 offset:12288
	v_pk_fma_f32 v[86:87], v[16:17], v[92:93], v[86:87]
	s_waitcnt lgkmcnt(0)
	v_pk_fma_f32 v[82:83], v[30:31], v[82:83], 0 op_sel_hi:[1,1,0]
	v_add_f32_e32 v94, v86, v87
	ds_read_b128 v[86:89], v70 offset:15360
	ds_read_b128 v[90:93], v70 offset:14336
	v_pk_fma_f32 v[82:83], v[24:25], v[84:85], v[82:83]
	s_nop 0
	v_pk_fma_f32 v[78:79], v[28:29], v[78:79], v[82:83]
	s_nop 0
	v_pk_fma_f32 v[78:79], v[20:21], v[80:81], v[78:79]
	s_waitcnt lgkmcnt(0)
	v_pk_fma_f32 v[78:79], v[26:27], v[90:91], v[78:79]
	s_nop 0
	v_pk_fma_f32 v[78:79], v[18:19], v[92:93], v[78:79]
	s_nop 0
	v_pk_fma_f32 v[78:79], v[22:23], v[86:87], v[78:79]
	s_nop 0
	v_pk_fma_f32 v[78:79], v[16:17], v[88:89], v[78:79]
	s_nop 0
	v_add_f32_e32 v95, v78, v79
	ds_read_b128 v[78:81], v70 offset:16384
	ds_read_b128 v[82:85], v70 offset:17408
	ds_read_b128 v[86:89], v70 offset:18432
	ds_read_b128 v[90:93], v70 offset:19456
	s_waitcnt lgkmcnt(3)
	v_pk_fma_f32 v[78:79], v[30:31], v[78:79], 0 op_sel_hi:[1,1,0]
	s_nop 0
	v_pk_fma_f32 v[78:79], v[24:25], v[80:81], v[78:79]
	s_waitcnt lgkmcnt(2)
	v_pk_fma_f32 v[78:79], v[28:29], v[82:83], v[78:79]
	s_nop 0
	v_pk_fma_f32 v[78:79], v[20:21], v[84:85], v[78:79]
	s_waitcnt lgkmcnt(1)
	v_pk_fma_f32 v[78:79], v[26:27], v[86:87], v[78:79]
	s_nop 0
	v_pk_fma_f32 v[78:79], v[18:19], v[88:89], v[78:79]
	s_waitcnt lgkmcnt(0)
	v_pk_fma_f32 v[86:87], v[22:23], v[90:91], v[78:79]
	ds_read_b128 v[78:81], v70 offset:21504
	ds_read_b128 v[82:85], v70 offset:20480
	v_pk_fma_f32 v[86:87], v[16:17], v[92:93], v[86:87]
	s_waitcnt lgkmcnt(0)
	v_pk_fma_f32 v[82:83], v[30:31], v[82:83], 0 op_sel_hi:[1,1,0]
	v_add_f32_e32 v96, v86, v87
	ds_read_b128 v[86:89], v70 offset:23552
	ds_read_b128 v[90:93], v70 offset:22528
	v_pk_fma_f32 v[82:83], v[24:25], v[84:85], v[82:83]
	s_nop 0
	v_pk_fma_f32 v[78:79], v[28:29], v[78:79], v[82:83]
	s_nop 0
	v_pk_fma_f32 v[78:79], v[20:21], v[80:81], v[78:79]
	s_waitcnt lgkmcnt(0)
	v_pk_fma_f32 v[78:79], v[26:27], v[90:91], v[78:79]
	s_nop 0
	v_pk_fma_f32 v[78:79], v[18:19], v[92:93], v[78:79]
	s_nop 0
	v_pk_fma_f32 v[78:79], v[22:23], v[86:87], v[78:79]
	s_nop 0
	v_pk_fma_f32 v[78:79], v[16:17], v[88:89], v[78:79]
	s_nop 0
	v_add_f32_e32 v97, v78, v79
	ds_read_b128 v[78:81], v70 offset:24576
	ds_read_b128 v[82:85], v70 offset:25600
	ds_read_b128 v[86:89], v70 offset:26624
	ds_read_b128 v[90:93], v70 offset:27648
	s_waitcnt lgkmcnt(3)
	v_pk_fma_f32 v[78:79], v[30:31], v[78:79], 0 op_sel_hi:[1,1,0]
	s_nop 0
	v_pk_fma_f32 v[78:79], v[24:25], v[80:81], v[78:79]
	s_waitcnt lgkmcnt(2)
	v_pk_fma_f32 v[78:79], v[28:29], v[82:83], v[78:79]
	s_nop 0
	v_pk_fma_f32 v[78:79], v[20:21], v[84:85], v[78:79]
	s_waitcnt lgkmcnt(1)
	v_pk_fma_f32 v[78:79], v[26:27], v[86:87], v[78:79]
	s_nop 0
	v_pk_fma_f32 v[78:79], v[18:19], v[88:89], v[78:79]
	s_waitcnt lgkmcnt(0)
	v_pk_fma_f32 v[86:87], v[22:23], v[90:91], v[78:79]
	ds_read_b128 v[78:81], v70 offset:29696
	ds_read_b128 v[82:85], v70 offset:28672
	v_pk_fma_f32 v[86:87], v[16:17], v[92:93], v[86:87]
	s_waitcnt lgkmcnt(0)
	v_pk_fma_f32 v[30:31], v[30:31], v[82:83], 0 op_sel_hi:[1,1,0]
	v_add_f32_e32 v98, v86, v87
	ds_read_b128 v[86:89], v70 offset:31744
	ds_read_b128 v[90:93], v70 offset:30720
	v_pk_fma_f32 v[24:25], v[24:25], v[84:85], v[30:31]
	s_nop 0
	v_pk_fma_f32 v[24:25], v[28:29], v[78:79], v[24:25]
	s_nop 0
	v_pk_fma_f32 v[20:21], v[20:21], v[80:81], v[24:25]
	s_waitcnt lgkmcnt(0)
	v_pk_fma_f32 v[20:21], v[26:27], v[90:91], v[20:21]
	s_nop 0
	v_pk_fma_f32 v[18:19], v[18:19], v[92:93], v[20:21]
	s_nop 0
	v_pk_fma_f32 v[18:19], v[22:23], v[86:87], v[18:19]
	s_nop 0
	v_pk_fma_f32 v[16:17], v[16:17], v[88:89], v[18:19]
	s_nop 0
	v_add_f32_e32 v16, v16, v17
	s_waitcnt lgkmcnt(0)
	s_nop 1
	v_permlane32_swap_b32_e32 v45, v96
	v_add_f32_e32 v17, v45, v96
	s_waitcnt lgkmcnt(0)
	s_nop 1
	v_permlane32_swap_b32_e32 v77, v97
	v_add_f32_e32 v19, v77, v97
	s_waitcnt lgkmcnt(0)
	s_nop 1
	v_permlane32_swap_b32_e32 v94, v98
	v_add_f32_e32 v18, v94, v98
	s_waitcnt lgkmcnt(0)
	s_nop 1
	v_permlane32_swap_b32_e32 v95, v16
	v_add_f32_e32 v16, v95, v16
	s_waitcnt lgkmcnt(0)
	s_nop 1
	v_permlane16_swap_b32_e32 v17, v18
	v_add_f32_e32 v17, v17, v18
	s_waitcnt lgkmcnt(0)
	s_nop 1
	v_permlane16_swap_b32_e32 v19, v16
	v_add_f32_e32 v16, v19, v16
	v_cndmask_b32_e64 v18, v17, v16, s[6:7]
	s_nop 1
	v_mov_b32_dpp v18, v18 row_ror:8 row_mask:0xf bank_mask:0xf
	v_cndmask_b32_e64 v16, v16, v17, s[6:7]
	s_waitcnt lgkmcnt(0)
	v_add_f32_e32 v16, v16, v18
	s_nop 1
	v_mov_b32_dpp v17, v16 quad_perm:[3,2,1,0] row_mask:0xf bank_mask:0xf
	s_nop 1
	v_mov_b32_dpp v17, v17 row_half_mirror row_mask:0xf bank_mask:0xf
	s_waitcnt lgkmcnt(0)
	v_add_f32_e32 v16, v16, v17
	s_nop 1
	v_mov_b32_dpp v17, v16 quad_perm:[2,3,0,1] row_mask:0xf bank_mask:0xf
	s_waitcnt lgkmcnt(0)
	v_add_f32_e32 v16, v16, v17
	s_nop 1
	v_mov_b32_dpp v17, v16 quad_perm:[1,0,3,2] row_mask:0xf bank_mask:0xf
	s_and_saveexec_b64 s[10:11], s[8:9]
	s_cbranch_execz .LBB0_102
	global_load_dword v18, v[42:43], off
	s_waitcnt lgkmcnt(0)
	v_add_f32_e32 v16, v16, v17
	s_sub_u32 s16, s16, s37
	s_subb_u32 s17, s17, s38
	s_waitcnt vmcnt(0)
	v_add_f32_e32 v16, v16, v18
	v_mul_f32_e64 v17, |v16|, s30
	v_exp_f32_e32 v30, v17
	v_min_f32_e32 v31, 0, v16
	v_add_f32_e32 v18, 1.0, v30
	v_add_f32_e32 v19, -1.0, v18
	v_frexp_mant_f32_e32 v20, v18
	v_cvt_f64_f32_e32 v[16:17], v18
	v_sub_f32_e32 v21, v19, v18
	v_frexp_exp_i32_f64_e32 v16, v[16:17]
	v_cmp_gt_f32_e32 vcc, s31, v20
	v_sub_f32_e32 v19, v30, v19
	v_add_f32_e32 v17, 1.0, v21
	v_subbrev_co_u32_e32 v16, vcc, 0, v16, vcc
	v_add_f32_e32 v17, v19, v17
	v_sub_u32_e32 v19, 0, v16
	v_ldexp_f32 v18, v18, v19
	v_add_f32_e32 v20, -1.0, v18
	v_add_f32_e32 v21, 1.0, v18
	v_ldexp_f32 v17, v17, v19
	v_add_f32_e32 v19, 1.0, v20
	v_add_f32_e32 v22, -1.0, v21
	v_sub_f32_e32 v19, v18, v19
	v_sub_f32_e32 v18, v18, v22
	v_add_f32_e32 v22, v17, v19
	v_add_f32_e32 v17, v17, v18
	v_add_f32_e32 v24, v21, v17
	v_rcp_f32_e32 v25, v24
	v_add_f32_e32 v19, v20, v22
	v_sub_f32_e32 v20, v19, v20
	v_sub_f32_e32 v18, v24, v21
	v_mul_f32_e32 v27, v19, v25
	v_sub_f32_e32 v26, v22, v20
	v_mul_f32_e32 v20, v24, v27
	v_sub_f32_e32 v17, v17, v18
	v_fma_f32 v22, v27, v24, -v20
	v_fmac_f32_e32 v22, v27, v17
	v_add_f32_e32 v18, v20, v22
	v_sub_f32_e32 v21, v19, v18
	v_mov_b32_e32 v23, v18
	v_pk_add_f32 v[18:19], v[18:19], v[20:21] neg_lo:[0,1] neg_hi:[0,1]
	v_cvt_f32_i32_e32 v16, v16
	v_pk_add_f32 v[18:19], v[18:19], v[22:23] neg_lo:[0,1] neg_hi:[0,1]
	v_cmp_neq_f32_e32 vcc, s34, v30
	v_add_f32_e32 v19, v26, v19
	v_add_f32_e32 v18, v18, v19
	v_add_f32_e32 v19, v21, v18
	v_mul_f32_e32 v23, v25, v19
	v_mul_f32_e32 v20, v24, v23
	v_sub_f32_e32 v21, v21, v19
	v_add_f32_e32 v28, v27, v23
	v_fma_f32 v22, v23, v24, -v20
	v_add_f32_e32 v26, v18, v21
	v_sub_f32_e32 v18, v28, v27
	v_fmac_f32_e32 v22, v23, v17
	v_sub_f32_e32 v17, v23, v18
	v_add_f32_e32 v18, v20, v22
	v_sub_f32_e32 v21, v19, v18
	v_mov_b32_e32 v23, v18
	v_pk_add_f32 v[18:19], v[18:19], v[20:21] neg_lo:[0,1] neg_hi:[0,1]
	s_nop 0
	v_pk_add_f32 v[18:19], v[18:19], v[22:23] neg_lo:[0,1] neg_hi:[0,1]
	s_nop 0
	v_add_f32_e32 v19, v26, v19
	v_add_f32_e32 v18, v18, v19
	v_add_f32_e32 v18, v21, v18
	v_mul_f32_e32 v18, v25, v18
	v_add_f32_e32 v17, v17, v18
	v_add_f32_e32 v18, v28, v17
	v_mul_f32_e32 v20, v18, v18
	v_sub_f32_e32 v21, v18, v28
	v_fmamk_f32 v22, v20, 0x3e9b6dac, v72
	v_sub_f32_e32 v21, v17, v21
	v_mul_f32_e32 v17, v18, v20
	v_fmaak_f32 v45, v20, v22, 0x3f2aaada
	v_ldexp_f32 v23, v21, 1
	v_pk_mul_f32 v[20:21], v[16:17], v[44:45]
	v_ldexp_f32 v19, v18, 1
	v_fma_f32 v18, v16, s33, -v20
	v_fmac_f32_e32 v18, 0xb102e308, v16
	v_pk_add_f32 v[16:17], v[20:21], v[18:19]
	v_mov_b32_e32 v22, v20
	v_sub_f32_e32 v26, v17, v19
	v_pk_add_f32 v[24:25], v[16:17], v[20:21] neg_lo:[0,1] neg_hi:[0,1]
	v_sub_f32_e32 v20, v21, v26
	v_add_f32_e32 v23, v23, v20
	v_pk_add_f32 v[20:21], v[16:17], v[22:23]
	v_mov_b32_e32 v19, v16
	v_mov_b32_e32 v25, v21
	v_pk_add_f32 v[28:29], v[18:19], v[24:25] neg_lo:[0,1] neg_hi:[0,1]
	v_pk_add_f32 v[18:19], v[18:19], v[24:25]
	v_mov_b32_e32 v27, v16
	v_pk_add_f32 v[24:25], v[18:19], v[16:17] op_sel:[1,0] op_sel_hi:[0,1] neg_lo:[0,1] neg_hi:[0,1]
	v_mov_b32_e32 v26, v23
	v_mov_b32_e32 v22, v21
	v_mov_b32_e32 v23, v19
	v_pk_mov_b32 v[16:17], v[16:17], v[24:25] op_sel:[1,0]
	v_pk_add_f32 v[20:21], v[20:21], v[24:25] op_sel_hi:[1,0] neg_lo:[0,1] neg_hi:[0,1]
	v_pk_add_f32 v[16:17], v[22:23], v[16:17] neg_lo:[0,1] neg_hi:[0,1]
	v_mov_b32_e32 v20, v28
	v_pk_add_f32 v[16:17], v[26:27], v[16:17] neg_lo:[0,1] neg_hi:[0,1]
	v_mov_b32_e32 v29, v19
	v_pk_add_f32 v[20:21], v[20:21], v[16:17]
	s_nop 0
	v_pk_add_f32 v[22:23], v[20:21], v[20:21] op_sel:[0,1] op_sel_hi:[1,0]
	s_nop 0
	v_pk_add_f32 v[18:19], v[18:19], v[22:23] op_sel:[1,0] op_sel_hi:[0,1]
	v_mov_b32_e32 v21, v18
	v_mov_b32_e32 v17, v22
	v_pk_add_f32 v[22:23], v[20:21], v[28:29] neg_lo:[0,1] neg_hi:[0,1]
	s_nop 0
	v_sub_f32_e32 v19, v20, v22
	v_pk_add_f32 v[16:17], v[16:17], v[22:23] neg_lo:[0,1] neg_hi:[0,1]
	v_sub_f32_e32 v19, v28, v19
	v_add_f32_e32 v16, v16, v19
	v_add_f32_e32 v16, v16, v17
	v_add_f32_e32 v16, v18, v16
	v_cndmask_b32_e32 v16, v74, v16, vcc
	v_cmp_ngt_f32_e32 vcc, -1.0, v30
	s_nop 1
	v_cndmask_b32_e32 v16, v75, v16, vcc
	v_cmp_neq_f32_e32 vcc, -1.0, v30
	s_nop 1
	v_cndmask_b32_e32 v16, v76, v16, vcc
	v_cmp_lt_f32_e64 vcc, |v30|, s35
	s_nop 1
	v_cndmask_b32_e32 v16, v16, v30, vcc
	v_sub_f32_e32 v18, v31, v16
	v_lshl_add_u64 v[16:17], s[16:17], 2, v[46:47]
	global_store_dword v[16:17], v18, off offset:4
	s_branch .LBB0_102

.LBB0_504:
	v_add_u32_e32 v126, 0, v235
	s_waitcnt lgkmcnt(0)
	ds_read_b128 v[0:3], v126
	ds_read_b128 v[4:7], v126 offset:1024
	ds_read_b128 v[8:11], v126 offset:2048
	ds_read_b128 v[12:15], v126 offset:3072
	ds_read_b128 v[16:19], v126 offset:4096
	s_waitcnt lgkmcnt(4)
	v_pk_fma_f32 v[20:21], v[146:147], v[0:1], 0 op_sel_hi:[1,1,0]
	ds_read_b128 v[24:27], v126 offset:6144
	v_pk_fma_f32 v[20:21], v[144:145], v[2:3], v[20:21]
	s_waitcnt lgkmcnt(1)
	v_pk_fma_f32 v[28:29], v[146:147], v[16:17], 0 op_sel_hi:[1,1,0]
	v_pk_fma_f32 v[20:21], v[150:151], v[4:5], v[20:21]
	v_pk_fma_f32 v[32:33], v[144:145], v[18:19], v[28:29]
	v_pk_fma_f32 v[20:21], v[148:149], v[6:7], v[20:21]
	ds_read_b128 v[28:31], v126 offset:7168
	v_pk_fma_f32 v[20:21], v[154:155], v[8:9], v[20:21]
	s_nop 0
	v_pk_fma_f32 v[20:21], v[152:153], v[10:11], v[20:21]
	s_nop 0
	v_pk_fma_f32 v[20:21], v[158:159], v[12:13], v[20:21]
	s_nop 0
	v_pk_fma_f32 v[208:209], v[156:157], v[14:15], v[20:21]
	ds_read_b128 v[20:23], v126 offset:5120
	s_waitcnt lgkmcnt(0)
	v_pk_fma_f32 v[32:33], v[150:151], v[20:21], v[32:33]
	s_nop 0
	v_pk_fma_f32 v[32:33], v[148:149], v[22:23], v[32:33]
	s_nop 0
	v_pk_fma_f32 v[32:33], v[154:155], v[24:25], v[32:33]
	s_nop 0
	v_pk_fma_f32 v[32:33], v[152:153], v[26:27], v[32:33]
	s_nop 0
	v_pk_fma_f32 v[32:33], v[158:159], v[28:29], v[32:33]
	s_nop 0
	v_pk_fma_f32 v[238:239], v[156:157], v[30:31], v[32:33]
	ds_read_b128 v[32:35], v126 offset:8192
	ds_read_b128 v[36:39], v126 offset:9216
	ds_read_b128 v[40:43], v126 offset:10240
	ds_read_b128 v[44:47], v126 offset:11264
	ds_read_b128 v[48:51], v126 offset:12288
	s_waitcnt lgkmcnt(4)
	v_pk_fma_f32 v[52:53], v[146:147], v[32:33], 0 op_sel_hi:[1,1,0]
	ds_read_b128 v[56:59], v126 offset:14336
	v_pk_fma_f32 v[52:53], v[144:145], v[34:35], v[52:53]
	s_waitcnt lgkmcnt(1)
	v_pk_fma_f32 v[60:61], v[146:147], v[48:49], 0 op_sel_hi:[1,1,0]
	v_pk_fma_f32 v[52:53], v[150:151], v[36:37], v[52:53]
	v_pk_fma_f32 v[64:65], v[144:145], v[50:51], v[60:61]
	v_pk_fma_f32 v[52:53], v[148:149], v[38:39], v[52:53]
	ds_read_b128 v[60:63], v126 offset:15360
	v_pk_fma_f32 v[52:53], v[154:155], v[40:41], v[52:53]
	s_nop 0
	v_pk_fma_f32 v[52:53], v[152:153], v[42:43], v[52:53]
	s_nop 0
	v_pk_fma_f32 v[52:53], v[158:159], v[44:45], v[52:53]
	s_nop 0
	v_pk_fma_f32 v[240:241], v[156:157], v[46:47], v[52:53]
	ds_read_b128 v[52:55], v126 offset:13312
	s_waitcnt lgkmcnt(0)
	v_pk_fma_f32 v[64:65], v[150:151], v[52:53], v[64:65]
	s_nop 0
	v_pk_fma_f32 v[64:65], v[148:149], v[54:55], v[64:65]
	s_nop 0
	v_pk_fma_f32 v[64:65], v[154:155], v[56:57], v[64:65]
	s_nop 0
	v_pk_fma_f32 v[64:65], v[152:153], v[58:59], v[64:65]
	s_nop 0
	v_pk_fma_f32 v[64:65], v[158:159], v[60:61], v[64:65]
	s_nop 0
	v_pk_fma_f32 v[242:243], v[156:157], v[62:63], v[64:65]
	ds_read_b128 v[64:67], v126 offset:16384
	ds_read_b128 v[68:71], v126 offset:17408
	ds_read_b128 v[72:75], v126 offset:18432
	ds_read_b128 v[76:79], v126 offset:19456
	ds_read_b128 v[80:83], v126 offset:20480
	s_waitcnt lgkmcnt(4)
	v_pk_fma_f32 v[84:85], v[146:147], v[64:65], 0 op_sel_hi:[1,1,0]
	ds_read_b128 v[88:91], v126 offset:22528
	v_pk_fma_f32 v[84:85], v[144:145], v[66:67], v[84:85]
	s_waitcnt lgkmcnt(1)
	v_pk_fma_f32 v[92:93], v[146:147], v[80:81], 0 op_sel_hi:[1,1,0]
	v_pk_fma_f32 v[84:85], v[150:151], v[68:69], v[84:85]
	v_pk_fma_f32 v[96:97], v[144:145], v[82:83], v[92:93]
	v_pk_fma_f32 v[84:85], v[148:149], v[70:71], v[84:85]
	ds_read_b128 v[92:95], v126 offset:23552
	v_pk_fma_f32 v[84:85], v[154:155], v[72:73], v[84:85]
	s_nop 0
	v_pk_fma_f32 v[84:85], v[152:153], v[74:75], v[84:85]
	s_nop 0
	v_pk_fma_f32 v[84:85], v[158:159], v[76:77], v[84:85]
	s_nop 0
	v_pk_fma_f32 v[244:245], v[156:157], v[78:79], v[84:85]
	ds_read_b128 v[84:87], v126 offset:21504
	s_waitcnt lgkmcnt(0)
	v_pk_fma_f32 v[96:97], v[150:151], v[84:85], v[96:97]
	s_nop 0
	v_pk_fma_f32 v[96:97], v[148:149], v[86:87], v[96:97]
	s_nop 0
	v_pk_fma_f32 v[96:97], v[154:155], v[88:89], v[96:97]
	s_nop 0
	v_pk_fma_f32 v[96:97], v[152:153], v[90:91], v[96:97]
	s_nop 0
	v_pk_fma_f32 v[96:97], v[158:159], v[92:93], v[96:97]
	s_nop 0
	v_pk_fma_f32 v[246:247], v[156:157], v[94:95], v[96:97]
	ds_read_b128 v[96:99], v126 offset:24576
	ds_read_b128 v[100:103], v126 offset:25600
	ds_read_b128 v[104:107], v126 offset:26624
	ds_read_b128 v[108:111], v126 offset:27648
	ds_read_b128 v[112:115], v126 offset:28672
	s_waitcnt lgkmcnt(4)
	v_pk_fma_f32 v[116:117], v[146:147], v[96:97], 0 op_sel_hi:[1,1,0]
	ds_read_b128 v[120:123], v126 offset:30720
	v_pk_fma_f32 v[116:117], v[144:145], v[98:99], v[116:117]
	s_waitcnt lgkmcnt(1)
	v_pk_fma_f32 v[124:125], v[146:147], v[112:113], 0 op_sel_hi:[1,1,0]
	v_pk_fma_f32 v[116:117], v[150:151], v[100:101], v[116:117]
	v_pk_fma_f32 v[250:251], v[144:145], v[114:115], v[124:125]
	v_pk_fma_f32 v[116:117], v[148:149], v[102:103], v[116:117]
	s_nop 0
	v_pk_fma_f32 v[116:117], v[154:155], v[104:105], v[116:117]
	s_nop 0
	v_pk_fma_f32 v[116:117], v[152:153], v[106:107], v[116:117]
	s_nop 0
	v_pk_fma_f32 v[116:117], v[158:159], v[108:109], v[116:117]
	s_nop 0
	v_pk_fma_f32 v[248:249], v[156:157], v[110:111], v[116:117]
	ds_read_b128 v[116:119], v126 offset:29696
	ds_read_b128 v[124:127], v126 offset:31744
	s_waitcnt lgkmcnt(1)
	v_pk_fma_f32 v[250:251], v[150:151], v[116:117], v[250:251]
	s_nop 0
	v_pk_fma_f32 v[250:251], v[148:149], v[118:119], v[250:251]
	s_nop 0
	v_pk_fma_f32 v[250:251], v[154:155], v[120:121], v[250:251]
	s_nop 0
	v_pk_fma_f32 v[250:251], v[152:153], v[122:123], v[250:251]
	s_waitcnt lgkmcnt(0)
	v_pk_fma_f32 v[250:251], v[158:159], v[124:125], v[250:251]
	s_nop 0
	v_pk_fma_f32 v[250:251], v[156:157], v[126:127], v[250:251]
	v_add_f32_e32 v208, v208, v209
	v_add_f32_e32 v209, v238, v239
	v_add_f32_e32 v239, v244, v245
	v_add_f32_e32 v237, v240, v241
	v_add_f32_e32 v238, v242, v243
	v_add_f32_e32 v241, v246, v247
	v_add_f32_e32 v242, v248, v249
	v_add_f32_e32 v243, v250, v251
	s_waitcnt lgkmcnt(0)
	s_nop 1
	v_permlane32_swap_b32_e32 v208, v239
	v_add_f32_e32 v208, v208, v239
	v_cndmask_b32_e64 v239, v209, v241, s[2:3]
	v_cndmask_b32_e64 v209, v241, v209, s[2:3]
	ds_bpermute_b32 v239, v220, v239
	s_waitcnt lgkmcnt(0)
	v_add_f32_e32 v209, v209, v239
	s_waitcnt lgkmcnt(0)
	s_nop 1
	v_permlane32_swap_b32_e32 v237, v242
	v_add_f32_e32 v237, v237, v242
	s_waitcnt lgkmcnt(0)
	s_nop 1
	v_permlane32_swap_b32_e32 v238, v243
	v_add_f32_e32 v238, v238, v243
	v_cndmask_b32_e64 v239, v208, v237, s[4:5]
	ds_bpermute_b32 v239, v219, v239
	v_cndmask_b32_e64 v208, v237, v208, s[4:5]
	s_waitcnt lgkmcnt(0)
	v_add_f32_e32 v208, v208, v239
	s_waitcnt lgkmcnt(0)
	s_nop 1
	v_permlane16_swap_b32_e32 v209, v238
	v_add_f32_e32 v209, v209, v238
	v_cndmask_b32_e64 v237, v208, v209, s[6:7]
	s_nop 1
	v_mov_b32_dpp v237, v237 row_ror:8 row_mask:0xf bank_mask:0xf
	v_cndmask_b32_e64 v208, v209, v208, s[6:7]
	s_waitcnt lgkmcnt(0)
	v_add_f32_e32 v208, v208, v237
	s_nop 1
	v_mov_b32_dpp v209, v208 quad_perm:[3,2,1,0] row_mask:0xf bank_mask:0xf
	s_nop 1
	v_mov_b32_dpp v209, v209 row_half_mirror row_mask:0xf bank_mask:0xf
	v_add_u32_e32 v237, 0, v236
	s_waitcnt lgkmcnt(0)
	v_add_f32_e32 v208, v208, v209
	s_nop 1
	v_mov_b32_dpp v209, v208 quad_perm:[2,3,0,1] row_mask:0xf bank_mask:0xf
	s_waitcnt lgkmcnt(0)
	v_add_f32_e32 v238, v208, v209
	s_nop 1
	v_mov_b32_dpp v239, v238 quad_perm:[1,0,3,2] row_mask:0xf bank_mask:0xf
	v_lshl_add_u64 v[208:209], v[138:139], 0, s[12:13]
	s_and_saveexec_b64 s[14:15], s[8:9]
	s_cbranch_execz .LBB0_506
	global_load_dword v240, v[208:209], off
	s_waitcnt lgkmcnt(0)
	v_add_f32_e32 v238, v238, v239
	v_add_u32_e32 v241, 0x20000, v237
	s_waitcnt vmcnt(0)
	v_add_f32_e32 v238, v238, v240
	ds_write_b32 v241, v238
.LBB0_506:
	s_or_b64 exec, exec, s[14:15]
	s_waitcnt lgkmcnt(0)
	v_pk_fma_f32 v[238:239], v[162:163], v[0:1], 0 op_sel_hi:[1,1,0]
	v_pk_fma_f32 v[240:241], v[162:163], v[16:17], 0 op_sel_hi:[1,1,0]
	v_pk_fma_f32 v[242:243], v[162:163], v[32:33], 0 op_sel_hi:[1,1,0]
	v_pk_fma_f32 v[246:247], v[162:163], v[64:65], 0 op_sel_hi:[1,1,0]
	v_pk_fma_f32 v[238:239], v[160:161], v[2:3], v[238:239]
	v_pk_fma_f32 v[240:241], v[160:161], v[18:19], v[240:241]
	v_pk_fma_f32 v[242:243], v[160:161], v[34:35], v[242:243]
	v_pk_fma_f32 v[246:247], v[160:161], v[66:67], v[246:247]
	v_pk_fma_f32 v[238:239], v[166:167], v[4:5], v[238:239]
	v_pk_fma_f32 v[240:241], v[166:167], v[20:21], v[240:241]
	v_pk_fma_f32 v[242:243], v[166:167], v[36:37], v[242:243]
	v_pk_fma_f32 v[246:247], v[166:167], v[68:69], v[246:247]
	v_pk_fma_f32 v[238:239], v[164:165], v[6:7], v[238:239]
	v_pk_fma_f32 v[240:241], v[164:165], v[22:23], v[240:241]
	v_pk_fma_f32 v[242:243], v[164:165], v[38:39], v[242:243]
	v_pk_fma_f32 v[246:247], v[164:165], v[70:71], v[246:247]
	v_pk_fma_f32 v[238:239], v[170:171], v[8:9], v[238:239]
	v_pk_fma_f32 v[240:241], v[170:171], v[24:25], v[240:241]
	v_pk_fma_f32 v[242:243], v[170:171], v[40:41], v[242:243]
	v_pk_fma_f32 v[246:247], v[170:171], v[72:73], v[246:247]
	v_pk_fma_f32 v[238:239], v[168:169], v[10:11], v[238:239]
	v_pk_fma_f32 v[240:241], v[168:169], v[26:27], v[240:241]
	v_pk_fma_f32 v[242:243], v[168:169], v[42:43], v[242:243]
	v_pk_fma_f32 v[246:247], v[168:169], v[74:75], v[246:247]
	v_pk_fma_f32 v[238:239], v[174:175], v[12:13], v[238:239]
	v_pk_fma_f32 v[240:241], v[174:175], v[28:29], v[240:241]
	v_pk_fma_f32 v[242:243], v[174:175], v[44:45], v[242:243]
	v_pk_fma_f32 v[244:245], v[162:163], v[48:49], 0 op_sel_hi:[1,1,0]
	v_pk_fma_f32 v[246:247], v[174:175], v[76:77], v[246:247]
	v_pk_fma_f32 v[248:249], v[162:163], v[80:81], 0 op_sel_hi:[1,1,0]
	v_pk_fma_f32 v[250:251], v[162:163], v[96:97], 0 op_sel_hi:[1,1,0]
	v_pk_fma_f32 v[252:253], v[162:163], v[112:113], 0 op_sel_hi:[1,1,0]
	v_pk_fma_f32 v[238:239], v[172:173], v[14:15], v[238:239]
	v_pk_fma_f32 v[240:241], v[172:173], v[30:31], v[240:241]
	v_pk_fma_f32 v[242:243], v[172:173], v[46:47], v[242:243]
	v_pk_fma_f32 v[244:245], v[160:161], v[50:51], v[244:245]
	v_pk_fma_f32 v[246:247], v[172:173], v[78:79], v[246:247]
	v_pk_fma_f32 v[248:249], v[160:161], v[82:83], v[248:249]
	v_pk_fma_f32 v[250:251], v[160:161], v[98:99], v[250:251]
	v_pk_fma_f32 v[252:253], v[160:161], v[114:115], v[252:253]
	v_pk_fma_f32 v[244:245], v[166:167], v[52:53], v[244:245]
	v_pk_fma_f32 v[248:249], v[166:167], v[84:85], v[248:249]
	v_pk_fma_f32 v[250:251], v[166:167], v[100:101], v[250:251]
	v_pk_fma_f32 v[252:253], v[166:167], v[116:117], v[252:253]
	v_add_f32_e32 v238, v238, v239
	v_add_f32_e32 v239, v240, v241
	v_add_f32_e32 v240, v242, v243
	v_add_f32_e32 v242, v246, v247
	v_pk_fma_f32 v[244:245], v[164:165], v[54:55], v[244:245]
	v_pk_fma_f32 v[248:249], v[164:165], v[86:87], v[248:249]
	v_pk_fma_f32 v[250:251], v[164:165], v[102:103], v[250:251]
	v_pk_fma_f32 v[252:253], v[164:165], v[118:119], v[252:253]
	v_pk_fma_f32 v[244:245], v[170:171], v[56:57], v[244:245]
	v_pk_fma_f32 v[248:249], v[170:171], v[88:89], v[248:249]
	v_pk_fma_f32 v[250:251], v[170:171], v[104:105], v[250:251]
	v_pk_fma_f32 v[252:253], v[170:171], v[120:121], v[252:253]
	v_pk_fma_f32 v[244:245], v[168:169], v[58:59], v[244:245]
	v_pk_fma_f32 v[248:249], v[168:169], v[90:91], v[248:249]
	v_pk_fma_f32 v[250:251], v[168:169], v[106:107], v[250:251]
	v_pk_fma_f32 v[252:253], v[168:169], v[122:123], v[252:253]
	v_pk_fma_f32 v[244:245], v[174:175], v[60:61], v[244:245]
	v_pk_fma_f32 v[248:249], v[174:175], v[92:93], v[248:249]
	v_pk_fma_f32 v[250:251], v[174:175], v[108:109], v[250:251]
	v_pk_fma_f32 v[252:253], v[174:175], v[124:125], v[252:253]
	v_pk_fma_f32 v[244:245], v[172:173], v[62:63], v[244:245]
	v_pk_fma_f32 v[248:249], v[172:173], v[94:95], v[248:249]
	v_pk_fma_f32 v[250:251], v[172:173], v[110:111], v[250:251]
	v_pk_fma_f32 v[252:253], v[172:173], v[126:127], v[252:253]
	v_add_f32_e32 v241, v244, v245
	v_add_f32_e32 v244, v248, v249
	v_add_f32_e32 v245, v250, v251
	v_add_f32_e32 v246, v252, v253
	s_waitcnt lgkmcnt(0)
	s_nop 1
	v_permlane32_swap_b32_e32 v238, v242
	v_add_f32_e32 v238, v238, v242
	v_cndmask_b32_e64 v242, v239, v244, s[2:3]
	v_cndmask_b32_e64 v239, v244, v239, s[2:3]
	ds_bpermute_b32 v242, v220, v242
	s_waitcnt lgkmcnt(0)
	v_add_f32_e32 v239, v239, v242
	s_waitcnt lgkmcnt(0)
	s_nop 1
	v_permlane32_swap_b32_e32 v240, v245
	v_add_f32_e32 v240, v240, v245
	s_waitcnt lgkmcnt(0)
	s_nop 1
	v_permlane32_swap_b32_e32 v241, v246
	v_add_f32_e32 v241, v241, v246
	s_waitcnt lgkmcnt(0)
	s_nop 1
	v_permlane16_swap_b32_e32 v238, v240
	v_add_f32_e32 v238, v238, v240
	s_waitcnt lgkmcnt(0)
	s_nop 1
	v_permlane16_swap_b32_e32 v239, v241
	v_add_f32_e32 v239, v239, v241
	v_cndmask_b32_e64 v240, v238, v239, s[6:7]
	s_nop 1
	v_mov_b32_dpp v240, v240 row_ror:8 row_mask:0xf bank_mask:0xf
	v_cndmask_b32_e64 v238, v239, v238, s[6:7]
	s_waitcnt lgkmcnt(0)
	v_add_f32_e32 v238, v238, v240
	s_nop 1
	v_mov_b32_dpp v239, v238 quad_perm:[3,2,1,0] row_mask:0xf bank_mask:0xf
	s_nop 1
	v_mov_b32_dpp v239, v239 row_half_mirror row_mask:0xf bank_mask:0xf
	s_waitcnt lgkmcnt(0)
	v_add_f32_e32 v238, v238, v239
	s_nop 1
	v_mov_b32_dpp v239, v238 quad_perm:[2,3,0,1] row_mask:0xf bank_mask:0xf
	s_waitcnt lgkmcnt(0)
	v_add_f32_e32 v238, v238, v239
	s_nop 1
	v_mov_b32_dpp v239, v238 quad_perm:[1,0,3,2] row_mask:0xf bank_mask:0xf
	s_and_saveexec_b64 s[14:15], s[8:9]
	s_cbranch_execz .LBB0_508
	global_load_dword v240, v[208:209], off
	s_waitcnt lgkmcnt(0)
	v_add_f32_e32 v238, v238, v239
	v_add_u32_e32 v241, 0x20080, v237
	s_waitcnt vmcnt(0)
	v_add_f32_e32 v238, v238, v240
	ds_write_b32 v241, v238
.LBB0_508:
	s_or_b64 exec, exec, s[14:15]
	s_waitcnt lgkmcnt(0)
	v_pk_fma_f32 v[238:239], v[178:179], v[0:1], 0 op_sel_hi:[1,1,0]
	v_pk_fma_f32 v[240:241], v[178:179], v[16:17], 0 op_sel_hi:[1,1,0]
	v_pk_fma_f32 v[242:243], v[178:179], v[32:33], 0 op_sel_hi:[1,1,0]
	v_pk_fma_f32 v[246:247], v[178:179], v[64:65], 0 op_sel_hi:[1,1,0]
	v_pk_fma_f32 v[238:239], v[176:177], v[2:3], v[238:239]
	v_pk_fma_f32 v[240:241], v[176:177], v[18:19], v[240:241]
	v_pk_fma_f32 v[242:243], v[176:177], v[34:35], v[242:243]
	v_pk_fma_f32 v[246:247], v[176:177], v[66:67], v[246:247]
	v_pk_fma_f32 v[238:239], v[182:183], v[4:5], v[238:239]
	v_pk_fma_f32 v[240:241], v[182:183], v[20:21], v[240:241]
	v_pk_fma_f32 v[242:243], v[182:183], v[36:37], v[242:243]
	v_pk_fma_f32 v[246:247], v[182:183], v[68:69], v[246:247]
	v_pk_fma_f32 v[238:239], v[180:181], v[6:7], v[238:239]
	v_pk_fma_f32 v[240:241], v[180:181], v[22:23], v[240:241]
	v_pk_fma_f32 v[242:243], v[180:181], v[38:39], v[242:243]
	v_pk_fma_f32 v[246:247], v[180:181], v[70:71], v[246:247]
	v_pk_fma_f32 v[238:239], v[186:187], v[8:9], v[238:239]
	v_pk_fma_f32 v[240:241], v[186:187], v[24:25], v[240:241]
	v_pk_fma_f32 v[242:243], v[186:187], v[40:41], v[242:243]
	v_pk_fma_f32 v[246:247], v[186:187], v[72:73], v[246:247]
	v_pk_fma_f32 v[238:239], v[184:185], v[10:11], v[238:239]
	v_pk_fma_f32 v[240:241], v[184:185], v[26:27], v[240:241]
	v_pk_fma_f32 v[242:243], v[184:185], v[42:43], v[242:243]
	v_pk_fma_f32 v[246:247], v[184:185], v[74:75], v[246:247]
	v_pk_fma_f32 v[238:239], v[190:191], v[12:13], v[238:239]
	v_pk_fma_f32 v[240:241], v[190:191], v[28:29], v[240:241]
	v_pk_fma_f32 v[242:243], v[190:191], v[44:45], v[242:243]
	v_pk_fma_f32 v[244:245], v[178:179], v[48:49], 0 op_sel_hi:[1,1,0]
	v_pk_fma_f32 v[246:247], v[190:191], v[76:77], v[246:247]
	v_pk_fma_f32 v[248:249], v[178:179], v[80:81], 0 op_sel_hi:[1,1,0]
	v_pk_fma_f32 v[250:251], v[178:179], v[96:97], 0 op_sel_hi:[1,1,0]
	v_pk_fma_f32 v[252:253], v[178:179], v[112:113], 0 op_sel_hi:[1,1,0]
	v_pk_fma_f32 v[238:239], v[188:189], v[14:15], v[238:239]
	v_pk_fma_f32 v[240:241], v[188:189], v[30:31], v[240:241]
	v_pk_fma_f32 v[242:243], v[188:189], v[46:47], v[242:243]
	v_pk_fma_f32 v[244:245], v[176:177], v[50:51], v[244:245]
	v_pk_fma_f32 v[246:247], v[188:189], v[78:79], v[246:247]
	v_pk_fma_f32 v[248:249], v[176:177], v[82:83], v[248:249]
	v_pk_fma_f32 v[250:251], v[176:177], v[98:99], v[250:251]
	v_pk_fma_f32 v[252:253], v[176:177], v[114:115], v[252:253]
	v_pk_fma_f32 v[244:245], v[182:183], v[52:53], v[244:245]
	v_pk_fma_f32 v[248:249], v[182:183], v[84:85], v[248:249]
	v_pk_fma_f32 v[250:251], v[182:183], v[100:101], v[250:251]
	v_pk_fma_f32 v[252:253], v[182:183], v[116:117], v[252:253]
	v_add_f32_e32 v238, v238, v239
	v_add_f32_e32 v239, v240, v241
	v_add_f32_e32 v240, v242, v243
	v_add_f32_e32 v242, v246, v247
	v_pk_fma_f32 v[244:245], v[180:181], v[54:55], v[244:245]
	v_pk_fma_f32 v[248:249], v[180:181], v[86:87], v[248:249]
	v_pk_fma_f32 v[250:251], v[180:181], v[102:103], v[250:251]
	v_pk_fma_f32 v[252:253], v[180:181], v[118:119], v[252:253]
	v_pk_fma_f32 v[244:245], v[186:187], v[56:57], v[244:245]
	v_pk_fma_f32 v[248:249], v[186:187], v[88:89], v[248:249]
	v_pk_fma_f32 v[250:251], v[186:187], v[104:105], v[250:251]
	v_pk_fma_f32 v[252:253], v[186:187], v[120:121], v[252:253]
	v_pk_fma_f32 v[244:245], v[184:185], v[58:59], v[244:245]
	v_pk_fma_f32 v[248:249], v[184:185], v[90:91], v[248:249]
	v_pk_fma_f32 v[250:251], v[184:185], v[106:107], v[250:251]
	v_pk_fma_f32 v[252:253], v[184:185], v[122:123], v[252:253]
	v_pk_fma_f32 v[244:245], v[190:191], v[60:61], v[244:245]
	v_pk_fma_f32 v[248:249], v[190:191], v[92:93], v[248:249]
	v_pk_fma_f32 v[250:251], v[190:191], v[108:109], v[250:251]
	v_pk_fma_f32 v[252:253], v[190:191], v[124:125], v[252:253]
	v_pk_fma_f32 v[244:245], v[188:189], v[62:63], v[244:245]
	v_pk_fma_f32 v[248:249], v[188:189], v[94:95], v[248:249]
	v_pk_fma_f32 v[250:251], v[188:189], v[110:111], v[250:251]
	v_pk_fma_f32 v[252:253], v[188:189], v[126:127], v[252:253]
	v_add_f32_e32 v241, v244, v245
	v_add_f32_e32 v244, v248, v249
	v_add_f32_e32 v245, v250, v251
	v_add_f32_e32 v246, v252, v253
	s_waitcnt lgkmcnt(0)
	s_nop 1
	v_permlane32_swap_b32_e32 v238, v242
	v_add_f32_e32 v238, v238, v242
	v_cndmask_b32_e64 v242, v239, v244, s[2:3]
	v_cndmask_b32_e64 v239, v244, v239, s[2:3]
	ds_bpermute_b32 v242, v220, v242
	s_waitcnt lgkmcnt(0)
	v_add_f32_e32 v239, v239, v242
	s_waitcnt lgkmcnt(0)
	s_nop 1
	v_permlane32_swap_b32_e32 v240, v245
	v_add_f32_e32 v240, v240, v245
	s_waitcnt lgkmcnt(0)
	s_nop 1
	v_permlane32_swap_b32_e32 v241, v246
	v_add_f32_e32 v241, v241, v246
	s_waitcnt lgkmcnt(0)
	s_nop 1
	v_permlane16_swap_b32_e32 v238, v240
	v_add_f32_e32 v238, v238, v240
	s_waitcnt lgkmcnt(0)
	s_nop 1
	v_permlane16_swap_b32_e32 v239, v241
	v_add_f32_e32 v239, v239, v241
	v_cndmask_b32_e64 v240, v238, v239, s[6:7]
	s_nop 1
	v_mov_b32_dpp v240, v240 row_ror:8 row_mask:0xf bank_mask:0xf
	v_cndmask_b32_e64 v238, v239, v238, s[6:7]
	s_waitcnt lgkmcnt(0)
	v_add_f32_e32 v238, v238, v240
	s_nop 1
	v_mov_b32_dpp v239, v238 quad_perm:[3,2,1,0] row_mask:0xf bank_mask:0xf
	s_nop 1
	v_mov_b32_dpp v239, v239 row_half_mirror row_mask:0xf bank_mask:0xf
	s_waitcnt lgkmcnt(0)
	v_add_f32_e32 v238, v238, v239
	s_nop 1
	v_mov_b32_dpp v239, v238 quad_perm:[2,3,0,1] row_mask:0xf bank_mask:0xf
	s_waitcnt lgkmcnt(0)
	v_add_f32_e32 v238, v238, v239
	s_nop 1
	v_mov_b32_dpp v239, v238 quad_perm:[1,0,3,2] row_mask:0xf bank_mask:0xf
	s_and_saveexec_b64 s[14:15], s[8:9]
	s_cbranch_execz .LBB0_510
	global_load_dword v240, v[208:209], off
	s_waitcnt lgkmcnt(0)
	v_add_f32_e32 v238, v238, v239
	v_add_u32_e32 v241, 0x20100, v237
	s_waitcnt vmcnt(0)
	v_add_f32_e32 v238, v238, v240
	ds_write_b32 v241, v238
.LBB0_510:
	s_or_b64 exec, exec, s[14:15]
	v_pk_fma_f32 v[0:1], v[194:195], v[0:1], 0 op_sel_hi:[1,1,0]
	s_nop 0
	v_pk_fma_f32 v[0:1], v[192:193], v[2:3], v[0:1]
	v_pk_fma_f32 v[2:3], v[194:195], v[16:17], 0 op_sel_hi:[1,1,0]
	v_pk_fma_f32 v[0:1], v[198:199], v[4:5], v[0:1]
	v_pk_fma_f32 v[4:5], v[194:195], v[32:33], 0 op_sel_hi:[1,1,0]
	v_pk_fma_f32 v[0:1], v[196:197], v[6:7], v[0:1]
	v_pk_fma_f32 v[2:3], v[192:193], v[18:19], v[2:3]
	v_pk_fma_f32 v[0:1], v[202:203], v[8:9], v[0:1]
	v_pk_fma_f32 v[8:9], v[194:195], v[64:65], 0 op_sel_hi:[1,1,0]
	v_pk_fma_f32 v[4:5], v[192:193], v[34:35], v[4:5]
	v_pk_fma_f32 v[8:9], v[192:193], v[66:67], v[8:9]
	v_pk_fma_f32 v[2:3], v[198:199], v[20:21], v[2:3]
	v_pk_fma_f32 v[4:5], v[198:199], v[36:37], v[4:5]
	v_pk_fma_f32 v[8:9], v[198:199], v[68:69], v[8:9]
	v_pk_fma_f32 v[2:3], v[196:197], v[22:23], v[2:3]
	v_pk_fma_f32 v[4:5], v[196:197], v[38:39], v[4:5]
	v_pk_fma_f32 v[8:9], v[196:197], v[70:71], v[8:9]
	v_pk_fma_f32 v[0:1], v[200:201], v[10:11], v[0:1]
	v_pk_fma_f32 v[2:3], v[202:203], v[24:25], v[2:3]
	v_pk_fma_f32 v[4:5], v[202:203], v[40:41], v[4:5]
	v_pk_fma_f32 v[8:9], v[202:203], v[72:73], v[8:9]
	v_pk_fma_f32 v[0:1], v[206:207], v[12:13], v[0:1]
	v_pk_fma_f32 v[2:3], v[200:201], v[26:27], v[2:3]
	v_pk_fma_f32 v[4:5], v[200:201], v[42:43], v[4:5]
	v_pk_fma_f32 v[8:9], v[200:201], v[74:75], v[8:9]
	v_pk_fma_f32 v[0:1], v[204:205], v[14:15], v[0:1]
	v_pk_fma_f32 v[2:3], v[206:207], v[28:29], v[2:3]
	v_pk_fma_f32 v[4:5], v[206:207], v[44:45], v[4:5]
	v_pk_fma_f32 v[6:7], v[194:195], v[48:49], 0 op_sel_hi:[1,1,0]
	v_pk_fma_f32 v[8:9], v[206:207], v[76:77], v[8:9]
	v_pk_fma_f32 v[10:11], v[194:195], v[80:81], 0 op_sel_hi:[1,1,0]
	v_pk_fma_f32 v[12:13], v[194:195], v[96:97], 0 op_sel_hi:[1,1,0]
	v_pk_fma_f32 v[14:15], v[194:195], v[112:113], 0 op_sel_hi:[1,1,0]
	v_pk_fma_f32 v[2:3], v[204:205], v[30:31], v[2:3]
	v_pk_fma_f32 v[4:5], v[204:205], v[46:47], v[4:5]
	v_pk_fma_f32 v[6:7], v[192:193], v[50:51], v[6:7]
	v_pk_fma_f32 v[8:9], v[204:205], v[78:79], v[8:9]
	v_pk_fma_f32 v[10:11], v[192:193], v[82:83], v[10:11]
	v_pk_fma_f32 v[12:13], v[192:193], v[98:99], v[12:13]
	v_pk_fma_f32 v[14:15], v[192:193], v[114:115], v[14:15]
	v_pk_fma_f32 v[6:7], v[198:199], v[52:53], v[6:7]
	v_pk_fma_f32 v[10:11], v[198:199], v[84:85], v[10:11]
	v_pk_fma_f32 v[12:13], v[198:199], v[100:101], v[12:13]
	v_pk_fma_f32 v[14:15], v[198:199], v[116:117], v[14:15]
	v_add_f32_e32 v0, v0, v1
	v_add_f32_e32 v1, v2, v3
	v_add_f32_e32 v2, v4, v5
	v_add_f32_e32 v4, v8, v9
	v_pk_fma_f32 v[6:7], v[196:197], v[54:55], v[6:7]
	v_pk_fma_f32 v[10:11], v[196:197], v[86:87], v[10:11]
	v_pk_fma_f32 v[12:13], v[196:197], v[102:103], v[12:13]
	v_pk_fma_f32 v[14:15], v[196:197], v[118:119], v[14:15]
	v_pk_fma_f32 v[6:7], v[202:203], v[56:57], v[6:7]
	v_pk_fma_f32 v[10:11], v[202:203], v[88:89], v[10:11]
	v_pk_fma_f32 v[12:13], v[202:203], v[104:105], v[12:13]
	v_pk_fma_f32 v[14:15], v[202:203], v[120:121], v[14:15]
	v_pk_fma_f32 v[6:7], v[200:201], v[58:59], v[6:7]
	v_pk_fma_f32 v[10:11], v[200:201], v[90:91], v[10:11]
	v_pk_fma_f32 v[12:13], v[200:201], v[106:107], v[12:13]
	v_pk_fma_f32 v[14:15], v[200:201], v[122:123], v[14:15]
	v_pk_fma_f32 v[6:7], v[206:207], v[60:61], v[6:7]
	v_pk_fma_f32 v[10:11], v[206:207], v[92:93], v[10:11]
	v_pk_fma_f32 v[12:13], v[206:207], v[108:109], v[12:13]
	v_pk_fma_f32 v[14:15], v[206:207], v[124:125], v[14:15]
	v_pk_fma_f32 v[6:7], v[204:205], v[62:63], v[6:7]
	v_pk_fma_f32 v[10:11], v[204:205], v[94:95], v[10:11]
	v_pk_fma_f32 v[12:13], v[204:205], v[110:111], v[12:13]
	v_pk_fma_f32 v[14:15], v[204:205], v[126:127], v[14:15]
	v_add_f32_e32 v3, v6, v7
	v_add_f32_e32 v6, v10, v11
	v_add_f32_e32 v7, v12, v13
	v_add_f32_e32 v8, v14, v15
	s_waitcnt lgkmcnt(0)
	s_nop 1
	v_permlane32_swap_b32_e32 v0, v4
	v_add_f32_e32 v0, v0, v4
	v_cndmask_b32_e64 v4, v1, v6, s[2:3]
	v_cndmask_b32_e64 v1, v6, v1, s[2:3]
	v_cndmask_b32_e64 v6, v3, v8, s[2:3]
	ds_bpermute_b32 v4, v220, v4
	ds_bpermute_b32 v6, v220, v6
	v_cndmask_b32_e64 v3, v8, v3, s[2:3]
	s_waitcnt lgkmcnt(1)
	v_add_f32_e32 v1, v1, v4
	s_waitcnt lgkmcnt(1)
	s_nop 1
	v_permlane32_swap_b32_e32 v2, v7
	v_add_f32_e32 v2, v2, v7
	s_waitcnt lgkmcnt(0)
	v_add_f32_e32 v3, v3, v6
	s_waitcnt lgkmcnt(0)
	s_nop 1
	v_permlane16_swap_b32_e32 v0, v2
	v_add_f32_e32 v0, v0, v2
	s_waitcnt lgkmcnt(0)
	s_nop 1
	v_permlane16_swap_b32_e32 v1, v3
	v_add_f32_e32 v1, v1, v3
	v_cndmask_b32_e64 v2, v0, v1, s[6:7]
	s_nop 1
	v_mov_b32_dpp v2, v2 row_ror:8 row_mask:0xf bank_mask:0xf
	v_cndmask_b32_e64 v0, v1, v0, s[6:7]
	s_waitcnt lgkmcnt(0)
	v_add_f32_e32 v0, v0, v2
	s_nop 1
	v_mov_b32_dpp v1, v0 quad_perm:[3,2,1,0] row_mask:0xf bank_mask:0xf
	s_nop 1
	v_mov_b32_dpp v1, v1 row_half_mirror row_mask:0xf bank_mask:0xf
	s_waitcnt lgkmcnt(0)
	v_add_f32_e32 v0, v0, v1
	s_nop 1
	v_mov_b32_dpp v1, v0 quad_perm:[2,3,0,1] row_mask:0xf bank_mask:0xf
	s_waitcnt lgkmcnt(0)
	v_add_f32_e32 v0, v0, v1
	s_nop 1
	v_mov_b32_dpp v1, v0 quad_perm:[1,0,3,2] row_mask:0xf bank_mask:0xf
	s_and_saveexec_b64 s[14:15], s[8:9]
	s_cbranch_execz .LBB0_503
	global_load_dword v2, v[208:209], off
	s_waitcnt lgkmcnt(0)
	v_add_f32_e32 v0, v0, v1
	v_add_u32_e32 v3, 0x20180, v237
	s_waitcnt vmcnt(0)
	v_add_f32_e32 v0, v0, v2
	ds_write_b32 v3, v0
	s_branch .LBB0_503

.LBB0_748:
	s_add_i32 s10, s40, s50
	s_add_i32 s24, s10, 2
	s_add_i32 s20, s10, 3
	s_add_i32 s10, s18, -7
	s_ashr_i32 s25, s24, 31
	s_ashr_i32 s21, s20, 31
	s_ashr_i32 s11, s10, 31
	s_lshl_b64 s[26:27], s[24:25], 11
	s_lshl_b64 s[22:23], s[20:21], 11
	s_lshl_b64 s[10:11], s[10:11], 2
	s_add_u32 s28, s33, s10
	s_addc_u32 s29, s34, s11
	s_add_u32 s10, s35, s10
	v_lshl_add_u64 v[72:73], v[34:35], 0, s[26:27]
	global_load_dword v82, v95, s[28:29]
	global_load_dwordx2 v[74:75], v[72:73], off nt
	s_addc_u32 s11, s36, s11
	s_add_i32 s28, s18, -6
	s_ashr_i32 s29, s28, 31
	s_lshl_b64 s[28:29], s[28:29], 2
	s_add_u32 s52, s33, s28
	s_addc_u32 s53, s34, s29
	global_load_dword v105, v95, s[52:53]
	s_add_u32 s28, s35, s28
	s_addc_u32 s29, s36, s29
	s_add_i32 s52, s18, -5
	s_ashr_i32 s53, s52, 31
	s_lshl_b64 s[52:53], s[52:53], 2
	s_add_u32 s54, s33, s52
	s_addc_u32 s55, s34, s53
	global_load_dword v113, v95, s[54:55]
	s_add_u32 s52, s35, s52
	s_addc_u32 s53, s36, s53
	s_add_i32 s54, s18, -4
	s_ashr_i32 s55, s54, 31
	s_lshl_b64 s[54:55], s[54:55], 2
	s_add_u32 s56, s33, s54
	s_addc_u32 s57, s34, s55
	s_add_u32 s54, s35, s54
	s_addc_u32 s55, s36, s55
	s_add_i32 s58, s18, -3
	s_ashr_i32 s59, s58, 31
	s_waitcnt lgkmcnt(0)
	v_lshl_add_u64 v[62:63], v[34:35], 0, s[22:23]
	global_load_dwordx2 v[76:77], v[72:73], off offset:512 nt
	global_load_dwordx2 v[78:79], v[72:73], off offset:1024 nt
	global_load_dwordx2 v[80:81], v[72:73], off offset:1536 nt
	global_load_dwordx2 v[70:71], v[62:63], off nt
	global_load_dwordx2 v[68:69], v[62:63], off offset:512 nt
	global_load_dwordx2 v[66:67], v[62:63], off offset:1024 nt
	global_load_dwordx2 v[64:65], v[62:63], off offset:1536 nt
	global_load_dword v112, v95, s[10:11]
	global_load_dword v126, v95, s[28:29]
	global_load_dword v127, v95, s[52:53]
	global_load_dword v114, v95, s[56:57]
	global_load_dword v128, v95, s[54:55]
	s_lshl_b64 s[10:11], s[58:59], 2
	s_add_u32 s28, s33, s10
	s_addc_u32 s29, s34, s11
	global_load_dword v115, v95, s[28:29]
	s_add_u32 s10, s35, s10
	s_addc_u32 s11, s36, s11
	s_add_i32 s28, s18, -2
	s_ashr_i32 s29, s28, 31
	s_lshl_b64 s[28:29], s[28:29], 2
	s_add_u32 s52, s33, s28
	s_addc_u32 s53, s34, s29
	s_add_u32 s28, s35, s28
	s_addc_u32 s29, s36, s29
	s_add_i32 s54, s18, -1
	s_ashr_i32 s55, s54, 31
	s_lshl_b64 s[54:55], s[54:55], 2
	s_add_u32 s56, s33, s54
	s_addc_u32 s57, s34, s55
	global_load_dword v116, v95, s[52:53]
	global_load_dword v132, v95, s[56:57]
	s_add_u32 s52, s35, s54
	s_addc_u32 s53, s36, s55
	s_ashr_i32 s19, s18, 31
	s_lshl_b64 s[54:55], s[18:19], 2
	s_add_u32 s56, s33, s54
	s_addc_u32 s57, s34, s55
	s_add_u32 s54, s35, s54
	s_addc_u32 s55, s36, s55
	s_waitcnt vmcnt(18)
	v_lshlrev_b32_sdwa v83, v98, v82 dst_sel:DWORD dst_unused:UNUSED_PAD src0_sel:DWORD src1_sel:BYTE_3
	v_add_u32_e32 v83, s45, v83
	ds_read_b32 v83, v83
	v_and_b32_e32 v82, 0xffffff, v82
	s_waitcnt vmcnt(17)
	v_and_b32_e32 v85, 0xffff0000, v74
	v_lshlrev_b32_e32 v86, 16, v75
	v_and_b32_e32 v87, 0xffff0000, v75
	s_waitcnt vmcnt(16)
	v_lshlrev_b32_sdwa v84, v98, v105 dst_sel:DWORD dst_unused:UNUSED_PAD src0_sel:DWORD src1_sel:BYTE_3
	v_add_u32_e32 v84, s45, v84
	ds_read_b32 v106, v84
	s_waitcnt lgkmcnt(1)
	v_add_u32_e32 v82, v83, v82
	v_ashrrev_i32_e32 v83, 31, v82
	v_lshlrev_b64 v[82:83], 10, v[82:83]
	v_lshl_add_u64 v[82:83], v[36:37], 0, v[82:83]
	global_load_dword v117, v[82:83], off nt
	global_load_dword v120, v[82:83], off offset:256 nt
	global_load_dword v124, v[82:83], off offset:512 nt
	global_load_dword v104, v95, s[10:11]
	global_load_dword v103, v95, s[28:29]
	global_load_dword v102, v95, s[52:53]
	global_load_dword v133, v95, s[56:57]
	global_load_dword v101, v95, s[54:55]
	v_lshlrev_b32_e32 v84, 16, v74
	v_and_b32_e32 v74, 0xffffff, v105
	global_load_dword v105, v[82:83], off offset:768 nt
	s_waitcnt vmcnt(24)
	v_lshlrev_b32_sdwa v75, v98, v113 dst_sel:DWORD dst_unused:UNUSED_PAD src0_sel:DWORD src1_sel:BYTE_3
	v_add_u32_e32 v75, s45, v75
	s_waitcnt lgkmcnt(0)
	v_add_u32_e32 v74, v106, v74
	ds_read_b32 v118, v75
	v_ashrrev_i32_e32 v75, 31, v74
	v_lshlrev_b64 v[74:75], 10, v[74:75]
	v_lshl_add_u64 v[74:75], v[36:37], 0, v[74:75]
	global_load_dword v129, v[74:75], off nt
	global_load_dword v130, v[74:75], off offset:256 nt
	global_load_dword v131, v[74:75], off offset:512 nt
	global_load_dword v134, v[74:75], off offset:768 nt
	s_waitcnt vmcnt(27)
	v_lshlrev_b32_e32 v82, 16, v76
	v_and_b32_e32 v83, 0xffff0000, v76
	v_and_b32_e32 v76, 0xffffff, v113
	s_waitcnt vmcnt(17)
	v_lshlrev_b32_sdwa v74, v98, v114 dst_sel:DWORD dst_unused:UNUSED_PAD src0_sel:DWORD src1_sel:BYTE_3
	s_waitcnt vmcnt(15)
	v_lshlrev_b32_sdwa v113, v98, v115 dst_sel:DWORD dst_unused:UNUSED_PAD src0_sel:DWORD src1_sel:BYTE_3
	v_add_u32_e32 v74, s45, v74
	v_add_u32_e32 v113, s45, v113
	v_lshlrev_b32_e32 v106, 16, v77
	v_and_b32_e32 v107, 0xffff0000, v77
	ds_read_b32 v77, v74
	ds_read_b32 v113, v113
	s_waitcnt lgkmcnt(2)
	v_add_u32_e32 v74, v118, v76
	v_ashrrev_i32_e32 v75, 31, v74
	v_lshlrev_b64 v[74:75], 10, v[74:75]
	v_lshl_add_u64 v[74:75], v[36:37], 0, v[74:75]
	global_load_dword v135, v[74:75], off nt
	global_load_dword v136, v[74:75], off offset:256 nt
	v_and_b32_e32 v76, 0xffffff, v114
	s_waitcnt lgkmcnt(1)
	v_add_u32_e32 v76, v77, v76
	v_ashrrev_i32_e32 v77, 31, v76
	v_lshlrev_b64 v[76:77], 10, v[76:77]
	v_lshl_add_u64 v[76:77], v[36:37], 0, v[76:77]
	global_load_dword v137, v[74:75], off offset:512 nt
	global_load_dword v138, v[74:75], off offset:768 nt
	global_load_dword v139, v[76:77], off nt
	global_load_dword v140, v[76:77], off offset:256 nt
	global_load_dword v141, v[76:77], off offset:512 nt
	global_load_dword v142, v[76:77], off offset:768 nt
	s_waitcnt vmcnt(22)
	v_lshlrev_b32_sdwa v74, v98, v116 dst_sel:DWORD dst_unused:UNUSED_PAD src0_sel:DWORD src1_sel:BYTE_3
	v_and_b32_e32 v114, 0xffffff, v115
	v_add_u32_e32 v74, s45, v74
	ds_read_b32 v77, v74
	s_waitcnt lgkmcnt(1)
	v_add_u32_e32 v74, v113, v114
	s_waitcnt vmcnt(21)
	v_lshlrev_b32_sdwa v113, v98, v132 dst_sel:DWORD dst_unused:UNUSED_PAD src0_sel:DWORD src1_sel:BYTE_3
	v_mul_f32_e32 v112, 0x3d000000, v112
	v_add_u32_e32 v113, s45, v113
	v_and_b32_e32 v76, 0xffffff, v116
	v_lshlrev_b32_e32 v108, 16, v78
	v_and_b32_e32 v109, 0xffff0000, v78
	v_lshlrev_b32_e32 v78, 16, v79
	v_and_b32_e32 v79, 0xffff0000, v79
	v_lshlrev_b32_e32 v110, 16, v80
	v_and_b32_e32 v111, 0xffff0000, v80
	ds_read_b32 v143, v113
	v_lshlrev_b32_e32 v80, 16, v81
	v_and_b32_e32 v81, 0xffff0000, v81
	v_ashrrev_i32_e32 v75, 31, v74
	s_waitcnt lgkmcnt(1)
	v_add_u32_e32 v76, v77, v76
	v_lshlrev_b64 v[74:75], 10, v[74:75]
	v_ashrrev_i32_e32 v77, 31, v76
	v_lshl_add_u64 v[74:75], v[36:37], 0, v[74:75]
	v_lshlrev_b64 v[76:77], 10, v[76:77]
	v_lshl_add_u64 v[76:77], v[36:37], 0, v[76:77]
	s_lshl_b64 s[28:29], s[24:25], 10
	s_waitcnt vmcnt(18)
	v_cvt_pk_f32_fp8_e32 v[122:123], v124
	v_cvt_pk_f32_fp8_sdwa v[124:125], v124 src0_sel:WORD_1
	v_cvt_pk_f32_fp8_e32 v[114:115], v117
	v_cvt_pk_f32_fp8_e32 v[118:119], v120
	v_cvt_pk_f32_fp8_sdwa v[120:121], v120 src0_sel:WORD_1
	v_cvt_pk_f32_fp8_sdwa v[116:117], v117 src0_sel:WORD_1
	v_pk_mul_f32 v[114:115], v[112:113], v[114:115] op_sel_hi:[0,1]
	v_pk_mul_f32 v[118:119], v[112:113], v[118:119] op_sel_hi:[0,1]
	v_pk_mul_f32 v[120:121], v[112:113], v[120:121] op_sel_hi:[0,1]
	v_pk_fma_f32 v[82:83], v[12:13], v[118:119], v[82:83]
	v_pk_fma_f32 v[106:107], v[14:15], v[120:121], v[106:107]
	s_waitcnt vmcnt(12)
	v_cvt_pk_f32_fp8_sdwa v[118:119], v105 src0_sel:WORD_1
	v_cvt_pk_f32_fp8_e32 v[120:121], v105
	v_pk_mul_f32 v[116:117], v[112:113], v[116:117] op_sel_hi:[0,1]
	v_pk_fma_f32 v[84:85], v[0:1], v[114:115], v[84:85]
	v_pk_mul_f32 v[114:115], v[112:113], v[124:125] op_sel_hi:[0,1]
	v_pk_fma_f32 v[86:87], v[2:3], v[116:117], v[86:87]
	v_pk_mul_f32 v[116:117], v[112:113], v[122:123] op_sel_hi:[0,1]
	v_pk_fma_f32 v[78:79], v[26:27], v[114:115], v[78:79]
	v_pk_mul_f32 v[114:115], v[112:113], v[118:119] op_sel_hi:[0,1]
	v_pk_mul_f32 v[112:113], v[112:113], v[120:121] op_sel_hi:[0,1]
	v_pk_fma_f32 v[108:109], v[24:25], v[116:117], v[108:109]
	v_pk_fma_f32 v[110:111], v[28:29], v[112:113], v[110:111]
	s_waitcnt vmcnt(11)
	v_cvt_pk_f32_fp8_e32 v[112:113], v129
	v_cvt_pk_f32_fp8_sdwa v[116:117], v129 src0_sel:WORD_1
	s_waitcnt vmcnt(10)
	v_cvt_pk_f32_fp8_e32 v[118:119], v130
	v_cvt_pk_f32_fp8_sdwa v[120:121], v130 src0_sel:WORD_1
	v_pk_fma_f32 v[80:81], v[30:31], v[114:115], v[80:81]
	v_mul_f32_e32 v114, 0x3d000000, v126
	v_pk_mul_f32 v[112:113], v[114:115], v[112:113] op_sel_hi:[0,1]
	v_pk_mul_f32 v[116:117], v[114:115], v[116:117] op_sel_hi:[0,1]
	v_pk_fma_f32 v[86:87], v[2:3], v[116:117], v[86:87]
	v_pk_fma_f32 v[84:85], v[0:1], v[112:113], v[84:85]
	v_pk_mul_f32 v[112:113], v[114:115], v[118:119] op_sel_hi:[0,1]
	v_pk_mul_f32 v[116:117], v[114:115], v[120:121] op_sel_hi:[0,1]
	s_waitcnt vmcnt(9)
	v_cvt_pk_f32_fp8_e32 v[118:119], v131
	v_cvt_pk_f32_fp8_sdwa v[120:121], v131 src0_sel:WORD_1
	v_pk_fma_f32 v[106:107], v[14:15], v[116:117], v[106:107]
	v_pk_fma_f32 v[82:83], v[12:13], v[112:113], v[82:83]
	v_pk_mul_f32 v[112:113], v[114:115], v[118:119] op_sel_hi:[0,1]
	v_pk_mul_f32 v[116:117], v[114:115], v[120:121] op_sel_hi:[0,1]
	s_waitcnt vmcnt(8)
	v_cvt_pk_f32_fp8_e32 v[118:119], v134
	v_cvt_pk_f32_fp8_sdwa v[120:121], v134 src0_sel:WORD_1
	v_pk_fma_f32 v[108:109], v[24:25], v[112:113], v[108:109]
	v_pk_fma_f32 v[78:79], v[26:27], v[116:117], v[78:79]
	v_pk_mul_f32 v[112:113], v[114:115], v[118:119] op_sel_hi:[0,1]
	v_pk_mul_f32 v[114:115], v[114:115], v[120:121] op_sel_hi:[0,1]
	v_pk_fma_f32 v[80:81], v[30:31], v[114:115], v[80:81]
	s_waitcnt vmcnt(7)
	v_cvt_pk_f32_fp8_sdwa v[114:115], v135 src0_sel:WORD_1
	v_cvt_pk_f32_fp8_e32 v[116:117], v135
	s_waitcnt vmcnt(6)
	v_cvt_pk_f32_fp8_sdwa v[118:119], v136 src0_sel:WORD_1
	v_cvt_pk_f32_fp8_e32 v[120:121], v136
	v_pk_fma_f32 v[110:111], v[28:29], v[112:113], v[110:111]
	v_mul_f32_e32 v112, 0x3d000000, v127
	v_pk_mul_f32 v[114:115], v[112:113], v[114:115] op_sel_hi:[0,1]
	v_pk_mul_f32 v[116:117], v[112:113], v[116:117] op_sel_hi:[0,1]
	v_pk_fma_f32 v[84:85], v[0:1], v[116:117], v[84:85]
	v_pk_fma_f32 v[86:87], v[2:3], v[114:115], v[86:87]
	v_pk_mul_f32 v[114:115], v[112:113], v[118:119] op_sel_hi:[0,1]
	v_pk_mul_f32 v[116:117], v[112:113], v[120:121] op_sel_hi:[0,1]
	s_waitcnt vmcnt(5)
	v_cvt_pk_f32_fp8_sdwa v[118:119], v137 src0_sel:WORD_1
	v_cvt_pk_f32_fp8_e32 v[120:121], v137
	v_pk_fma_f32 v[82:83], v[12:13], v[116:117], v[82:83]
	v_pk_fma_f32 v[106:107], v[14:15], v[114:115], v[106:107]
	v_pk_mul_f32 v[114:115], v[112:113], v[118:119] op_sel_hi:[0,1]
	v_pk_mul_f32 v[116:117], v[112:113], v[120:121] op_sel_hi:[0,1]
	s_waitcnt vmcnt(4)
	v_cvt_pk_f32_fp8_sdwa v[118:119], v138 src0_sel:WORD_1
	v_cvt_pk_f32_fp8_e32 v[120:121], v138
	v_pk_fma_f32 v[78:79], v[26:27], v[114:115], v[78:79]
	v_pk_fma_f32 v[108:109], v[24:25], v[116:117], v[108:109]
	v_pk_mul_f32 v[114:115], v[112:113], v[118:119] op_sel_hi:[0,1]
	v_pk_mul_f32 v[112:113], v[112:113], v[120:121] op_sel_hi:[0,1]
	v_pk_fma_f32 v[110:111], v[28:29], v[112:113], v[110:111]
	s_waitcnt vmcnt(3)
	v_cvt_pk_f32_fp8_e32 v[112:113], v139
	s_waitcnt vmcnt(2)
	v_cvt_pk_f32_fp8_e32 v[118:119], v140
	v_cvt_pk_f32_fp8_sdwa v[116:117], v139 src0_sel:WORD_1
	v_pk_fma_f32 v[80:81], v[30:31], v[114:115], v[80:81]
	v_mul_f32_e32 v114, 0x3d000000, v128
	v_cvt_pk_f32_fp8_sdwa v[120:121], v140 src0_sel:WORD_1
	v_pk_mul_f32 v[112:113], v[114:115], v[112:113] op_sel_hi:[0,1]
	v_pk_fma_f32 v[84:85], v[0:1], v[112:113], v[84:85]
	v_pk_mul_f32 v[112:113], v[114:115], v[118:119] op_sel_hi:[0,1]
	s_waitcnt vmcnt(1)
	v_cvt_pk_f32_fp8_e32 v[118:119], v141
	v_pk_mul_f32 v[116:117], v[114:115], v[116:117] op_sel_hi:[0,1]
	v_pk_fma_f32 v[86:87], v[2:3], v[116:117], v[86:87]
	v_pk_mul_f32 v[116:117], v[114:115], v[120:121] op_sel_hi:[0,1]
	v_cvt_pk_f32_fp8_sdwa v[120:121], v141 src0_sel:WORD_1
	v_pk_fma_f32 v[82:83], v[12:13], v[112:113], v[82:83]
	v_pk_mul_f32 v[112:113], v[114:115], v[118:119] op_sel_hi:[0,1]
	s_waitcnt vmcnt(0)
	v_cvt_pk_f32_fp8_e32 v[118:119], v142
	v_pk_fma_f32 v[106:107], v[14:15], v[116:117], v[106:107]
	v_pk_mul_f32 v[116:117], v[114:115], v[120:121] op_sel_hi:[0,1]
	v_cvt_pk_f32_fp8_sdwa v[120:121], v142 src0_sel:WORD_1
	v_pk_fma_f32 v[108:109], v[24:25], v[112:113], v[108:109]
	v_pk_mul_f32 v[112:113], v[114:115], v[118:119] op_sel_hi:[0,1]
	v_and_b32_sdwa v105, v85, v99 dst_sel:DWORD dst_unused:UNUSED_PAD src0_sel:WORD_1 src1_sel:DWORD
	v_pk_fma_f32 v[110:111], v[28:29], v[112:113], v[110:111]
	v_and_b32_sdwa v112, v84, v99 dst_sel:DWORD dst_unused:UNUSED_PAD src0_sel:WORD_1 src1_sel:DWORD
	v_add3_u32 v85, v85, v105, s46
	v_and_b32_sdwa v105, v87, v99 dst_sel:DWORD dst_unused:UNUSED_PAD src0_sel:WORD_1 src1_sel:DWORD
	v_pk_mul_f32 v[114:115], v[114:115], v[120:121] op_sel_hi:[0,1]
	v_add3_u32 v121, v84, v112, s46
	v_and_b32_sdwa v112, v86, v99 dst_sel:DWORD dst_unused:UNUSED_PAD src0_sel:WORD_1 src1_sel:DWORD
	v_add3_u32 v87, v87, v105, s46
	v_and_b32_sdwa v105, v83, v99 dst_sel:DWORD dst_unused:UNUSED_PAD src0_sel:WORD_1 src1_sel:DWORD
	v_add3_u32 v134, v86, v112, s46
	v_and_b32_sdwa v112, v82, v99 dst_sel:DWORD dst_unused:UNUSED_PAD src0_sel:WORD_1 src1_sel:DWORD
	v_add3_u32 v83, v83, v105, s46
	v_and_b32_sdwa v105, v107, v99 dst_sel:DWORD dst_unused:UNUSED_PAD src0_sel:WORD_1 src1_sel:DWORD
	v_add3_u32 v135, v82, v112, s46
	v_and_b32_sdwa v112, v106, v99 dst_sel:DWORD dst_unused:UNUSED_PAD src0_sel:WORD_1 src1_sel:DWORD
	v_add3_u32 v105, v107, v105, s46
	v_pk_fma_f32 v[78:79], v[26:27], v[116:117], v[78:79]
	v_add3_u32 v136, v106, v112, s46
	v_and_b32_e32 v123, 0xffff0000, v105
	v_and_b32_sdwa v105, v109, v99 dst_sel:DWORD dst_unused:UNUSED_PAD src0_sel:WORD_1 src1_sel:DWORD
	v_and_b32_sdwa v106, v108, v99 dst_sel:DWORD dst_unused:UNUSED_PAD src0_sel:WORD_1 src1_sel:DWORD
	v_add3_u32 v105, v109, v105, s46
	v_add3_u32 v137, v108, v106, s46
	v_and_b32_sdwa v106, v78, v99 dst_sel:DWORD dst_unused:UNUSED_PAD src0_sel:WORD_1 src1_sel:DWORD
	v_and_b32_e32 v125, 0xffff0000, v105
	v_and_b32_sdwa v105, v79, v99 dst_sel:DWORD dst_unused:UNUSED_PAD src0_sel:WORD_1 src1_sel:DWORD
	v_add3_u32 v138, v78, v106, s46
	v_and_b32_sdwa v78, v111, v99 dst_sel:DWORD dst_unused:UNUSED_PAD src0_sel:WORD_1 src1_sel:DWORD
	v_pk_fma_f32 v[80:81], v[30:31], v[114:115], v[80:81]
	v_add3_u32 v79, v79, v105, s46
	v_add3_u32 v78, v111, v78, s46
	v_and_b32_e32 v127, 0xffff0000, v79
	v_and_b32_sdwa v79, v110, v99 dst_sel:DWORD dst_unused:UNUSED_PAD src0_sel:WORD_1 src1_sel:DWORD
	v_and_b32_e32 v129, 0xffff0000, v78
	v_and_b32_sdwa v78, v81, v99 dst_sel:DWORD dst_unused:UNUSED_PAD src0_sel:WORD_1 src1_sel:DWORD
	v_and_b32_e32 v85, 0xffff0000, v85
	v_and_b32_e32 v84, 0xffff0000, v121
	v_add3_u32 v139, v110, v79, s46
	v_and_b32_sdwa v79, v80, v99 dst_sel:DWORD dst_unused:UNUSED_PAD src0_sel:WORD_1 src1_sel:DWORD
	v_add3_u32 v78, v81, v78, s46
	v_and_b32_e32 v87, 0xffff0000, v87
	v_and_b32_e32 v86, 0xffff0000, v134
	v_add3_u32 v80, v80, v79, s46
	v_and_b32_e32 v131, 0xffff0000, v78
	v_pk_fma_f32 v[78:79], v[84:85], v[84:85], 0 op_sel_hi:[1,1,0]
	v_and_b32_e32 v83, 0xffff0000, v83
	v_and_b32_e32 v82, 0xffff0000, v135
	v_pk_fma_f32 v[78:79], v[86:87], v[86:87], v[78:79]
	v_and_b32_e32 v122, 0xffff0000, v136
	v_pk_fma_f32 v[78:79], v[82:83], v[82:83], v[78:79]
	v_and_b32_e32 v124, 0xffff0000, v137
	v_pk_fma_f32 v[78:79], v[122:123], v[122:123], v[78:79]
	v_and_b32_e32 v126, 0xffff0000, v138
	v_pk_fma_f32 v[78:79], v[124:125], v[124:125], v[78:79]
	v_and_b32_e32 v128, 0xffff0000, v139
	v_pk_fma_f32 v[78:79], v[126:127], v[126:127], v[78:79]
	v_and_b32_e32 v130, 0xffff0000, v80
	v_pk_fma_f32 v[78:79], v[128:129], v[128:129], v[78:79]
	global_load_dword v120, v[74:75], off nt
	global_load_dword v119, v[74:75], off offset:256 nt
	global_load_dword v118, v[74:75], off offset:512 nt
	global_load_dword v117, v[74:75], off offset:768 nt
	global_load_dword v116, v[76:77], off nt
	global_load_dword v115, v[76:77], off offset:256 nt
	global_load_dword v113, v[76:77], off offset:512 nt
	global_load_dword v111, v[76:77], off offset:768 nt
	v_pk_fma_f32 v[78:79], v[130:131], v[130:131], v[78:79]
	v_lshlrev_b32_sdwa v77, v98, v133 dst_sel:DWORD dst_unused:UNUSED_PAD src0_sel:DWORD src1_sel:BYTE_3
	v_add_f32_e32 v78, v78, v79
	v_add_u32_e32 v77, s45, v77
	ds_read_b32 v77, v77
	v_and_b32_e32 v74, 0xffffff, v132
	s_waitcnt lgkmcnt(0)
	v_add_u32_e32 v74, v143, v74
	s_waitcnt lgkmcnt(0)
	s_nop 1
	v_add_f32_dpp v75, v78, v78 quad_perm:[1,0,3,2] row_mask:0xf bank_mask:0xf
	v_and_b32_e32 v79, 0xffffff, v133
	s_waitcnt lgkmcnt(0)
	s_nop 1
	v_add_f32_dpp v76, v75, v75 quad_perm:[2,3,0,1] row_mask:0xf bank_mask:0xf
	v_ashrrev_i32_e32 v75, 31, v74
	v_lshlrev_b64 v[74:75], 10, v[74:75]
	v_lshl_add_u64 v[74:75], v[36:37], 0, v[74:75]
	s_waitcnt lgkmcnt(0)
	s_nop 1
	v_add_f32_dpp v78, v76, v76 row_half_mirror row_mask:0xf bank_mask:0xf
	v_add_u32_e32 v76, v77, v79
	v_ashrrev_i32_e32 v77, 31, v76
	v_lshlrev_b64 v[76:77], 10, v[76:77]
	v_lshl_add_u64 v[76:77], v[36:37], 0, v[76:77]
	s_waitcnt lgkmcnt(0)
	s_nop 1
	v_add_f32_dpp v78, v78, v78 row_mirror row_mask:0xf bank_mask:0xf
	global_load_dword v114, v[74:75], off nt
	global_load_dword v112, v[74:75], off offset:256 nt
	global_load_dword v110, v[74:75], off offset:512 nt
	global_load_dword v109, v[74:75], off offset:768 nt
	global_load_dword v108, v[76:77], off nt
	global_load_dword v107, v[76:77], off offset:256 nt
	global_load_dword v106, v[76:77], off offset:512 nt
	global_load_dword v105, v[76:77], off offset:768 nt
	v_or_b32_sdwa v74, v85, v121 dst_sel:DWORD dst_unused:UNUSED_PAD src0_sel:DWORD src1_sel:WORD_1
	v_or_b32_sdwa v75, v87, v134 dst_sel:DWORD dst_unused:UNUSED_PAD src0_sel:DWORD src1_sel:WORD_1
	global_store_dwordx2 v[72:73], v[74:75], off
	s_waitcnt lgkmcnt(0)
	v_mov_b32_e32 v76, v78
	v_mov_b32_e32 v79, v78
	s_nop 1
	v_permlane16_swap_b32_e32 v76, v79
	v_add_f32_e32 v76, v76, v79
	v_or_b32_sdwa v74, v83, v135 dst_sel:DWORD dst_unused:UNUSED_PAD src0_sel:DWORD src1_sel:WORD_1
	v_or_b32_sdwa v75, v123, v136 dst_sel:DWORD dst_unused:UNUSED_PAD src0_sel:DWORD src1_sel:WORD_1
	global_store_dwordx2 v[72:73], v[74:75], off offset:512
	s_waitcnt lgkmcnt(0)
	v_mov_b32_e32 v74, v76
	v_mov_b32_e32 v77, v76
	s_nop 1
	v_permlane32_swap_b32_e32 v74, v77
	v_add_f32_e32 v74, v74, v77
	v_fmamk_f32 v74, v74, 0x3a800000, v96
	v_mul_f32_e32 v75, 0x4f800000, v74
	v_cmp_gt_f32_e32 vcc, s47, v74
	s_nop 1
	v_cndmask_b32_e32 v76, v74, v75, vcc
	v_sqrt_f32_e32 v77, v76
	v_or_b32_sdwa v74, v125, v137 dst_sel:DWORD dst_unused:UNUSED_PAD src0_sel:DWORD src1_sel:WORD_1
	v_or_b32_sdwa v75, v127, v138 dst_sel:DWORD dst_unused:UNUSED_PAD src0_sel:DWORD src1_sel:WORD_1
	global_store_dwordx2 v[72:73], v[74:75], off offset:1024
	v_add_u32_e32 v74, -1, v77
	v_fma_f32 v75, -v74, v77, v76
	v_cmp_ge_f32_e64 s[10:11], 0, v75
	v_add_u32_e32 v75, 1, v77
	s_nop 0
	v_cndmask_b32_e64 v74, v77, v74, s[10:11]
	v_fma_f32 v77, -v75, v77, v76
	v_cmp_lt_f32_e64 s[10:11], 0, v77
	s_nop 1
	v_cndmask_b32_e64 v74, v74, v75, s[10:11]
	v_mul_f32_e32 v75, 0x37800000, v74
	v_cndmask_b32_e32 v74, v74, v75, vcc
	v_cmp_class_f32_e32 vcc, v76, v97
	v_or_b32_sdwa v75, v131, v80 dst_sel:DWORD dst_unused:UNUSED_PAD src0_sel:DWORD src1_sel:WORD_1
	s_nop 0
	v_cndmask_b32_e32 v76, v74, v76, vcc
	v_div_scale_f32 v77, s[10:11], v76, v76, 1.0
	v_rcp_f32_e32 v78, v77
	v_or_b32_sdwa v74, v129, v139 dst_sel:DWORD dst_unused:UNUSED_PAD src0_sel:DWORD src1_sel:WORD_1
	global_store_dwordx2 v[72:73], v[74:75], off offset:1536
	v_fma_f32 v72, -v77, v78, 1.0
	v_fmac_f32_e32 v78, v72, v78
	v_div_scale_f32 v72, vcc, 1.0, v76, 1.0
	v_mul_f32_e32 v73, v72, v78
	v_fma_f32 v74, -v77, v73, v72
	v_fmac_f32_e32 v73, v74, v78
	v_fma_f32 v72, -v77, v73, v72
	v_div_fmas_f32 v72, v72, v78, v73
	v_div_fixup_f32 v132, v72, v76, 1.0
	v_pk_mul_f32 v[74:75], v[132:133], v[84:85] op_sel_hi:[0,1]
	v_pk_fma_f32 v[74:75], v[48:49], v[74:75], v[4:5]
	v_pk_mul_f32 v[72:73], v[132:133], v[86:87] op_sel_hi:[0,1]
	v_bfe_u32 v121, v74, 16, 1
	v_pk_mul_f32 v[78:79], v[132:133], v[82:83] op_sel_hi:[0,1]
	v_pk_mul_f32 v[82:83], v[132:133], v[124:125] op_sel_hi:[0,1]
	v_add3_u32 v121, v74, v121, s46
	v_bfe_u32 v124, v75, 16, 1
	v_pk_fma_f32 v[72:73], v[46:47], v[72:73], v[6:7]
	v_lshrrev_b32_e32 v121, 16, v121
	v_add3_u32 v124, v75, v124, s46
	v_and_or_b32 v124, v124, s44, v121
	v_bfe_u32 v121, v72, 16, 1
	v_add3_u32 v121, v72, v121, s46
	v_bfe_u32 v125, v73, 16, 1
	v_pk_fma_f32 v[78:79], v[52:53], v[78:79], v[8:9]
	v_lshrrev_b32_e32 v121, 16, v121
	v_add3_u32 v125, v73, v125, s46
	v_pk_mul_f32 v[76:77], v[132:133], v[122:123] op_sel_hi:[0,1]
	v_lshl_add_u64 v[122:123], v[38:39], 0, s[26:27]
	v_and_or_b32 v125, v125, s44, v121
	v_bfe_u32 v121, v78, 16, 1
	global_store_dwordx2 v[122:123], v[124:125], off
	v_add3_u32 v121, v78, v121, s46
	v_bfe_u32 v124, v79, 16, 1
	v_pk_fma_f32 v[76:77], v[50:51], v[76:77], v[10:11]
	v_lshrrev_b32_e32 v121, 16, v121
	v_add3_u32 v124, v79, v124, s46
	v_and_or_b32 v124, v124, s44, v121
	v_bfe_u32 v121, v76, 16, 1
	v_add3_u32 v121, v76, v121, s46
	v_bfe_u32 v125, v77, 16, 1
	v_pk_fma_f32 v[82:83], v[56:57], v[82:83], v[16:17]
	v_lshrrev_b32_e32 v121, 16, v121
	v_add3_u32 v125, v77, v125, s46
	v_and_or_b32 v125, v125, s44, v121
	v_bfe_u32 v121, v82, 16, 1
	v_pk_mul_f32 v[80:81], v[132:133], v[126:127] op_sel_hi:[0,1]
	global_store_dwordx2 v[122:123], v[124:125], off offset:512
	v_add3_u32 v121, v82, v121, s46
	v_bfe_u32 v124, v83, 16, 1
	v_pk_fma_f32 v[80:81], v[54:55], v[80:81], v[18:19]
	v_lshrrev_b32_e32 v121, 16, v121
	v_add3_u32 v124, v83, v124, s46
	v_and_or_b32 v124, v124, s44, v121
	v_bfe_u32 v121, v80, 16, 1
	v_pk_mul_f32 v[86:87], v[132:133], v[128:129] op_sel_hi:[0,1]
	v_add3_u32 v121, v80, v121, s46
	v_bfe_u32 v125, v81, 16, 1
	v_pk_fma_f32 v[86:87], v[60:61], v[86:87], v[20:21]
	v_lshrrev_b32_e32 v121, 16, v121
	v_add3_u32 v125, v81, v125, s46
	v_and_or_b32 v125, v125, s44, v121
	v_bfe_u32 v121, v86, 16, 1
	v_pk_mul_f32 v[84:85], v[132:133], v[130:131] op_sel_hi:[0,1]
	global_store_dwordx2 v[122:123], v[124:125], off offset:1024
	v_add3_u32 v121, v86, v121, s46
	v_bfe_u32 v124, v87, 16, 1
	v_pk_fma_f32 v[84:85], v[58:59], v[84:85], v[22:23]
	v_lshrrev_b32_e32 v121, 16, v121
	v_add3_u32 v124, v87, v124, s46
	v_and_or_b32 v124, v124, s44, v121
	v_bfe_u32 v121, v84, 16, 1
	v_add3_u32 v121, v84, v121, s46
	v_bfe_u32 v125, v85, 16, 1
	v_mul_f32_e32 v126, 0x41000000, v74
	v_mul_f32_e32 v127, 0x41000000, v75
	v_lshrrev_b32_e32 v121, 16, v121
	v_add3_u32 v125, v85, v125, s46
	v_med3_f32 v126, v126, s48, v100
	v_med3_f32 v127, v127, s48, v100
	v_mov_b32_e32 v129, 0
	v_cvt_pk_fp8_f32 v129, v126, v127
	v_and_or_b32 v125, v125, s44, v121
	v_mul_f32_e32 v128, 0x41000000, v72
	global_store_dwordx2 v[122:123], v[124:125], off offset:1536
	v_mul_f32_e32 v121, 0x41000000, v78
	v_mul_f32_e32 v122, 0x41000000, v79
	v_mul_f32_e32 v126, 0x41000000, v73
	v_med3_f32 v127, v128, s48, v100
	v_med3_f32 v121, v121, s48, v100
	v_med3_f32 v122, v122, s48, v100
	v_mov_b32_e32 v128, 0
	v_med3_f32 v126, v126, s48, v100
	v_cvt_pk_fp8_f32 v128, v121, v122
	v_cvt_pk_fp8_f32 v129, v127, v126 op_sel:[0,0,1]
	v_mul_f32_e32 v123, 0x41000000, v76
	v_mul_f32_e32 v121, 0x41000000, v77
	v_med3_f32 v122, v123, s48, v100
	v_med3_f32 v121, v121, s48, v100
	v_lshl_add_u64 v[126:127], v[40:41], 0, s[28:29]
	v_cvt_pk_fp8_f32 v128, v122, v121 op_sel:[0,0,1]
	v_mul_f32_e32 v121, 0x41000000, v82
	v_mul_f32_e32 v122, 0x41000000, v83
	global_store_dword v[126:127], v129, off
	v_med3_f32 v121, v121, s48, v100
	v_med3_f32 v122, v122, s48, v100
	v_mov_b32_e32 v129, 0
	v_cvt_pk_fp8_f32 v129, v121, v122
	v_mul_f32_e32 v123, 0x41000000, v80
	v_mul_f32_e32 v121, 0x41000000, v81
	v_med3_f32 v122, v123, s48, v100
	v_med3_f32 v121, v121, s48, v100
	v_cvt_pk_fp8_f32 v129, v122, v121 op_sel:[0,0,1]
	v_mul_f32_e32 v121, 0x41000000, v86
	v_mul_f32_e32 v122, 0x41000000, v87
	v_med3_f32 v121, v121, s48, v100
	v_med3_f32 v122, v122, s48, v100
	v_mov_b32_e32 v130, 0
	v_cvt_pk_fp8_f32 v130, v121, v122
	v_mul_f32_e32 v123, 0x41000000, v84
	v_mul_f32_e32 v121, 0x41000000, v85
	v_med3_f32 v122, v123, s48, v100
	v_med3_f32 v121, v121, s48, v100
	v_cvt_pk_fp8_f32 v130, v122, v121 op_sel:[0,0,1]
	ds_read_b128 v[122:125], v94
	global_store_dword v[126:127], v128, off offset:256
	global_store_dword v[126:127], v129, off offset:512
	global_store_dword v[126:127], v130, off offset:768
	ds_read_b128 v[126:129], v94 offset:1024
	ds_read_b128 v[130:133], v94 offset:2048
	s_waitcnt lgkmcnt(2)
	v_pk_fma_f32 v[122:123], v[74:75], v[122:123], 0 op_sel_hi:[1,1,0]
	s_nop 0
	v_pk_fma_f32 v[134:135], v[72:73], v[124:125], v[122:123]
	ds_read_b128 v[122:125], v94 offset:3072
	s_waitcnt lgkmcnt(2)
	v_pk_fma_f32 v[126:127], v[78:79], v[126:127], v[134:135]
	s_nop 0
	v_pk_fma_f32 v[126:127], v[76:77], v[128:129], v[126:127]
	s_waitcnt lgkmcnt(1)
	v_pk_fma_f32 v[126:127], v[82:83], v[130:131], v[126:127]
	s_nop 0
	v_pk_fma_f32 v[126:127], v[80:81], v[132:133], v[126:127]
	s_waitcnt lgkmcnt(0)
	v_pk_fma_f32 v[122:123], v[86:87], v[122:123], v[126:127]
	ds_read_b128 v[126:129], v94 offset:5120
	ds_read_b128 v[130:133], v94 offset:4096
	v_pk_fma_f32 v[122:123], v[84:85], v[124:125], v[122:123]
	s_waitcnt lgkmcnt(0)
	v_pk_fma_f32 v[130:131], v[74:75], v[130:131], 0 op_sel_hi:[1,1,0]
	v_add_f32_e32 v121, v122, v123
	ds_read_b128 v[122:125], v94 offset:7168
	ds_read_b128 v[134:137], v94 offset:6144
	v_pk_fma_f32 v[130:131], v[72:73], v[132:133], v[130:131]
	s_nop 0
	v_pk_fma_f32 v[126:127], v[78:79], v[126:127], v[130:131]
	s_nop 0
	v_pk_fma_f32 v[126:127], v[76:77], v[128:129], v[126:127]
	s_waitcnt lgkmcnt(0)
	v_pk_fma_f32 v[126:127], v[82:83], v[134:135], v[126:127]
	s_nop 0
	v_pk_fma_f32 v[126:127], v[80:81], v[136:137], v[126:127]
	s_nop 0
	v_pk_fma_f32 v[122:123], v[86:87], v[122:123], v[126:127]
	s_nop 0
	v_pk_fma_f32 v[122:123], v[84:85], v[124:125], v[122:123]
	s_nop 0
	v_add_f32_e32 v138, v122, v123
	ds_read_b128 v[122:125], v94 offset:8192
	ds_read_b128 v[126:129], v94 offset:9216
	ds_read_b128 v[130:133], v94 offset:10240
	ds_read_b128 v[134:137], v94 offset:11264
	s_waitcnt lgkmcnt(3)
	v_pk_fma_f32 v[122:123], v[74:75], v[122:123], 0 op_sel_hi:[1,1,0]
	s_nop 0
	v_pk_fma_f32 v[122:123], v[72:73], v[124:125], v[122:123]
	s_waitcnt lgkmcnt(2)
	v_pk_fma_f32 v[122:123], v[78:79], v[126:127], v[122:123]
	s_nop 0
	v_pk_fma_f32 v[122:123], v[76:77], v[128:129], v[122:123]
	s_waitcnt lgkmcnt(1)
	v_pk_fma_f32 v[122:123], v[82:83], v[130:131], v[122:123]
	s_nop 0
	v_pk_fma_f32 v[122:123], v[80:81], v[132:133], v[122:123]
	s_waitcnt lgkmcnt(0)
	v_pk_fma_f32 v[130:131], v[86:87], v[134:135], v[122:123]
	ds_read_b128 v[122:125], v94 offset:13312
	ds_read_b128 v[126:129], v94 offset:12288
	v_pk_fma_f32 v[130:131], v[84:85], v[136:137], v[130:131]
	s_waitcnt lgkmcnt(0)
	v_pk_fma_f32 v[126:127], v[74:75], v[126:127], 0 op_sel_hi:[1,1,0]
	v_add_f32_e32 v139, v130, v131
	ds_read_b128 v[130:133], v94 offset:15360
	ds_read_b128 v[134:137], v94 offset:14336
	v_pk_fma_f32 v[126:127], v[72:73], v[128:129], v[126:127]
	s_nop 0
	v_pk_fma_f32 v[122:123], v[78:79], v[122:123], v[126:127]
	s_nop 0
	v_pk_fma_f32 v[122:123], v[76:77], v[124:125], v[122:123]
	s_waitcnt lgkmcnt(0)
	v_pk_fma_f32 v[122:123], v[82:83], v[134:135], v[122:123]
	s_nop 0
	v_pk_fma_f32 v[122:123], v[80:81], v[136:137], v[122:123]
	s_nop 0
	v_pk_fma_f32 v[122:123], v[86:87], v[130:131], v[122:123]
	s_nop 0
	v_pk_fma_f32 v[122:123], v[84:85], v[132:133], v[122:123]
	s_nop 0
	v_add_f32_e32 v140, v122, v123
	ds_read_b128 v[122:125], v94 offset:16384
	ds_read_b128 v[126:129], v94 offset:17408
	ds_read_b128 v[130:133], v94 offset:18432
	ds_read_b128 v[134:137], v94 offset:19456
	s_waitcnt lgkmcnt(3)
	v_pk_fma_f32 v[122:123], v[74:75], v[122:123], 0 op_sel_hi:[1,1,0]
	s_nop 0
	v_pk_fma_f32 v[122:123], v[72:73], v[124:125], v[122:123]
	s_waitcnt lgkmcnt(2)
	v_pk_fma_f32 v[122:123], v[78:79], v[126:127], v[122:123]
	s_nop 0
	v_pk_fma_f32 v[122:123], v[76:77], v[128:129], v[122:123]
	s_waitcnt lgkmcnt(1)
	v_pk_fma_f32 v[122:123], v[82:83], v[130:131], v[122:123]
	s_nop 0
	v_pk_fma_f32 v[122:123], v[80:81], v[132:133], v[122:123]
	s_waitcnt lgkmcnt(0)
	v_pk_fma_f32 v[130:131], v[86:87], v[134:135], v[122:123]
	ds_read_b128 v[122:125], v94 offset:21504
	ds_read_b128 v[126:129], v94 offset:20480
	v_pk_fma_f32 v[130:131], v[84:85], v[136:137], v[130:131]
	s_waitcnt lgkmcnt(0)
	v_pk_fma_f32 v[126:127], v[74:75], v[126:127], 0 op_sel_hi:[1,1,0]
	v_add_f32_e32 v141, v130, v131
	ds_read_b128 v[130:133], v94 offset:23552
	ds_read_b128 v[134:137], v94 offset:22528
	v_pk_fma_f32 v[126:127], v[72:73], v[128:129], v[126:127]
	s_nop 0
	v_pk_fma_f32 v[122:123], v[78:79], v[122:123], v[126:127]
	s_nop 0
	v_pk_fma_f32 v[122:123], v[76:77], v[124:125], v[122:123]
	s_waitcnt lgkmcnt(0)
	v_pk_fma_f32 v[122:123], v[82:83], v[134:135], v[122:123]
	s_nop 0
	v_pk_fma_f32 v[122:123], v[80:81], v[136:137], v[122:123]
	s_nop 0
	v_pk_fma_f32 v[122:123], v[86:87], v[130:131], v[122:123]
	s_nop 0
	v_pk_fma_f32 v[122:123], v[84:85], v[132:133], v[122:123]
	s_nop 0
	v_add_f32_e32 v142, v122, v123
	ds_read_b128 v[122:125], v94 offset:24576
	ds_read_b128 v[126:129], v94 offset:25600
	ds_read_b128 v[130:133], v94 offset:26624
	ds_read_b128 v[134:137], v94 offset:27648
	s_waitcnt lgkmcnt(3)
	v_pk_fma_f32 v[122:123], v[74:75], v[122:123], 0 op_sel_hi:[1,1,0]
	s_nop 0
	v_pk_fma_f32 v[122:123], v[72:73], v[124:125], v[122:123]
	s_waitcnt lgkmcnt(2)
	v_pk_fma_f32 v[122:123], v[78:79], v[126:127], v[122:123]
	s_nop 0
	v_pk_fma_f32 v[122:123], v[76:77], v[128:129], v[122:123]
	s_waitcnt lgkmcnt(1)
	v_pk_fma_f32 v[122:123], v[82:83], v[130:131], v[122:123]
	s_nop 0
	v_pk_fma_f32 v[122:123], v[80:81], v[132:133], v[122:123]
	s_waitcnt lgkmcnt(0)
	v_pk_fma_f32 v[130:131], v[86:87], v[134:135], v[122:123]
	ds_read_b128 v[122:125], v94 offset:29696
	ds_read_b128 v[126:129], v94 offset:28672
	v_pk_fma_f32 v[130:131], v[84:85], v[136:137], v[130:131]
	s_waitcnt lgkmcnt(0)
	v_pk_fma_f32 v[74:75], v[74:75], v[126:127], 0 op_sel_hi:[1,1,0]
	v_add_f32_e32 v143, v130, v131
	ds_read_b128 v[130:133], v94 offset:31744
	ds_read_b128 v[134:137], v94 offset:30720
	v_pk_fma_f32 v[72:73], v[72:73], v[128:129], v[74:75]
	s_nop 0
	v_pk_fma_f32 v[72:73], v[78:79], v[122:123], v[72:73]
	s_nop 0
	v_pk_fma_f32 v[72:73], v[76:77], v[124:125], v[72:73]
	s_waitcnt lgkmcnt(0)
	v_pk_fma_f32 v[72:73], v[82:83], v[134:135], v[72:73]
	s_nop 0
	v_pk_fma_f32 v[72:73], v[80:81], v[136:137], v[72:73]
	s_nop 0
	v_pk_fma_f32 v[72:73], v[86:87], v[130:131], v[72:73]
	s_nop 0
	v_pk_fma_f32 v[72:73], v[84:85], v[132:133], v[72:73]
	s_nop 0
	v_add_f32_e32 v72, v72, v73
	s_waitcnt lgkmcnt(0)
	s_nop 1
	v_permlane32_swap_b32_e32 v121, v141
	v_add_f32_e32 v73, v121, v141
	s_waitcnt lgkmcnt(0)
	s_nop 1
	v_permlane32_swap_b32_e32 v138, v142
	v_add_f32_e32 v75, v138, v142
	s_waitcnt lgkmcnt(0)
	s_nop 1
	v_permlane32_swap_b32_e32 v139, v143
	v_add_f32_e32 v74, v139, v143
	s_waitcnt lgkmcnt(0)
	s_nop 1
	v_permlane32_swap_b32_e32 v140, v72
	v_add_f32_e32 v72, v140, v72
	s_waitcnt lgkmcnt(0)
	s_nop 1
	v_permlane16_swap_b32_e32 v73, v74
	v_add_f32_e32 v73, v73, v74
	s_waitcnt lgkmcnt(0)
	s_nop 1
	v_permlane16_swap_b32_e32 v75, v72
	v_add_f32_e32 v72, v75, v72
	v_cndmask_b32_e64 v74, v73, v72, s[6:7]
	s_nop 1
	v_mov_b32_dpp v74, v74 row_ror:8 row_mask:0xf bank_mask:0xf
	v_cndmask_b32_e64 v72, v72, v73, s[6:7]
	s_waitcnt lgkmcnt(0)
	v_add_f32_e32 v72, v72, v74
	s_nop 1
	v_mov_b32_dpp v73, v72 quad_perm:[3,2,1,0] row_mask:0xf bank_mask:0xf
	s_nop 1
	v_mov_b32_dpp v73, v73 row_half_mirror row_mask:0xf bank_mask:0xf
	s_waitcnt lgkmcnt(0)
	v_add_f32_e32 v72, v72, v73
	s_nop 1
	v_mov_b32_dpp v73, v72 quad_perm:[2,3,0,1] row_mask:0xf bank_mask:0xf
	s_waitcnt lgkmcnt(0)
	v_add_f32_e32 v72, v72, v73
	s_nop 1
	v_mov_b32_dpp v73, v72 quad_perm:[1,0,3,2] row_mask:0xf bank_mask:0xf
	s_and_saveexec_b64 s[10:11], s[8:9]
	s_cbranch_execz .LBB0_750
	s_lshl_b64 s[24:25], s[24:25], 5
	v_lshl_add_u64 v[74:75], v[42:43], 0, s[24:25]
	s_waitcnt lgkmcnt(0)
	v_add_f32_e32 v72, v72, v73
	global_store_dword v[74:75], v72, off
.LBB0_750:
	s_or_b64 exec, exec, s[10:11]
	s_waitcnt vmcnt(27)
	v_cvt_pk_f32_fp8_sdwa v[80:81], v120 src0_sel:WORD_1
	s_waitcnt vmcnt(26)
	v_cvt_pk_f32_fp8_sdwa v[86:87], v119 src0_sel:WORD_1
	v_cvt_pk_f32_fp8_e32 v[82:83], v120
	v_mul_f32_e32 v84, 0x3d000000, v104
	v_lshlrev_b32_e32 v72, 16, v70
	s_waitcnt lgkmcnt(0)
	v_and_b32_e32 v73, 0xffff0000, v70
	v_lshlrev_b32_e32 v70, 16, v71
	v_and_b32_e32 v71, 0xffff0000, v71
	v_pk_mul_f32 v[80:81], v[84:85], v[80:81] op_sel_hi:[0,1]
	v_cvt_pk_f32_fp8_e32 v[120:121], v119
	v_pk_fma_f32 v[70:71], v[2:3], v[80:81], v[70:71]
	v_pk_mul_f32 v[80:81], v[84:85], v[86:87] op_sel_hi:[0,1]
	s_waitcnt vmcnt(25)
	v_cvt_pk_f32_fp8_sdwa v[86:87], v118 src0_sel:WORD_1
	v_cvt_pk_f32_fp8_e32 v[118:119], v118
	v_pk_mul_f32 v[82:83], v[84:85], v[82:83] op_sel_hi:[0,1]
	v_lshlrev_b32_e32 v74, 16, v68
	v_and_b32_e32 v75, 0xffff0000, v68
	v_pk_fma_f32 v[72:73], v[0:1], v[82:83], v[72:73]
	v_pk_mul_f32 v[82:83], v[84:85], v[120:121] op_sel_hi:[0,1]
	v_lshlrev_b32_e32 v68, 16, v69
	v_and_b32_e32 v69, 0xffff0000, v69
	v_pk_fma_f32 v[74:75], v[12:13], v[82:83], v[74:75]
	v_pk_mul_f32 v[82:83], v[84:85], v[118:119] op_sel_hi:[0,1]
	s_waitcnt vmcnt(24)
	v_cvt_pk_f32_fp8_e32 v[118:119], v117
	v_pk_fma_f32 v[68:69], v[14:15], v[80:81], v[68:69]
	v_pk_mul_f32 v[80:81], v[84:85], v[86:87] op_sel_hi:[0,1]
	v_cvt_pk_f32_fp8_sdwa v[86:87], v117 src0_sel:WORD_1
	v_lshlrev_b32_e32 v76, 16, v66
	v_and_b32_e32 v77, 0xffff0000, v66
	v_lshlrev_b32_e32 v66, 16, v67
	v_and_b32_e32 v67, 0xffff0000, v67
	v_lshlrev_b32_e32 v78, 16, v64
	v_and_b32_e32 v79, 0xffff0000, v64
	v_pk_fma_f32 v[76:77], v[24:25], v[82:83], v[76:77]
	v_pk_mul_f32 v[82:83], v[84:85], v[118:119] op_sel_hi:[0,1]
	v_pk_fma_f32 v[66:67], v[26:27], v[80:81], v[66:67]
	v_pk_mul_f32 v[80:81], v[84:85], v[86:87] op_sel_hi:[0,1]
	v_pk_fma_f32 v[78:79], v[28:29], v[82:83], v[78:79]
	s_waitcnt vmcnt(23)
	v_cvt_pk_f32_fp8_e32 v[82:83], v116
	v_cvt_pk_f32_fp8_sdwa v[84:85], v116 src0_sel:WORD_1
	s_waitcnt vmcnt(22)
	v_cvt_pk_f32_fp8_e32 v[86:87], v115
	v_cvt_pk_f32_fp8_sdwa v[116:117], v115 src0_sel:WORD_1
	v_lshlrev_b32_e32 v64, 16, v65
	v_and_b32_e32 v65, 0xffff0000, v65
	v_pk_fma_f32 v[64:65], v[30:31], v[80:81], v[64:65]
	v_mul_f32_e32 v80, 0x3d000000, v103
	v_pk_mul_f32 v[82:83], v[80:81], v[82:83] op_sel_hi:[0,1]
	v_pk_mul_f32 v[84:85], v[80:81], v[84:85] op_sel_hi:[0,1]
	v_pk_fma_f32 v[70:71], v[2:3], v[84:85], v[70:71]
	v_pk_fma_f32 v[72:73], v[0:1], v[82:83], v[72:73]
	v_pk_mul_f32 v[82:83], v[80:81], v[86:87] op_sel_hi:[0,1]
	v_pk_mul_f32 v[84:85], v[80:81], v[116:117] op_sel_hi:[0,1]
	s_waitcnt vmcnt(21)
	v_cvt_pk_f32_fp8_e32 v[86:87], v113
	v_cvt_pk_f32_fp8_sdwa v[116:117], v113 src0_sel:WORD_1
	v_pk_fma_f32 v[68:69], v[14:15], v[84:85], v[68:69]
	v_pk_fma_f32 v[74:75], v[12:13], v[82:83], v[74:75]
	v_pk_mul_f32 v[82:83], v[80:81], v[86:87] op_sel_hi:[0,1]
	v_pk_mul_f32 v[84:85], v[80:81], v[116:117] op_sel_hi:[0,1]
	s_waitcnt vmcnt(20)
	v_cvt_pk_f32_fp8_e32 v[86:87], v111
	v_cvt_pk_f32_fp8_sdwa v[116:117], v111 src0_sel:WORD_1
	v_pk_fma_f32 v[76:77], v[24:25], v[82:83], v[76:77]
	v_pk_fma_f32 v[66:67], v[26:27], v[84:85], v[66:67]
	v_pk_mul_f32 v[82:83], v[80:81], v[86:87] op_sel_hi:[0,1]
	v_pk_mul_f32 v[80:81], v[80:81], v[116:117] op_sel_hi:[0,1]
	v_pk_fma_f32 v[64:65], v[30:31], v[80:81], v[64:65]
	s_waitcnt vmcnt(19)
	v_cvt_pk_f32_fp8_sdwa v[80:81], v114 src0_sel:WORD_1
	v_cvt_pk_f32_fp8_e32 v[84:85], v114
	v_pk_fma_f32 v[78:79], v[28:29], v[82:83], v[78:79]
	v_mul_f32_e32 v82, 0x3d000000, v102
	s_waitcnt vmcnt(18)
	v_cvt_pk_f32_fp8_sdwa v[86:87], v112 src0_sel:WORD_1
	v_cvt_pk_f32_fp8_e32 v[102:103], v112
	v_pk_mul_f32 v[80:81], v[82:83], v[80:81] op_sel_hi:[0,1]
	v_pk_mul_f32 v[84:85], v[82:83], v[84:85] op_sel_hi:[0,1]
	v_pk_fma_f32 v[72:73], v[0:1], v[84:85], v[72:73]
	v_pk_fma_f32 v[70:71], v[2:3], v[80:81], v[70:71]
	v_pk_mul_f32 v[80:81], v[82:83], v[86:87] op_sel_hi:[0,1]
	v_pk_mul_f32 v[84:85], v[82:83], v[102:103] op_sel_hi:[0,1]
	s_waitcnt vmcnt(17)
	v_cvt_pk_f32_fp8_sdwa v[86:87], v110 src0_sel:WORD_1
	v_cvt_pk_f32_fp8_e32 v[102:103], v110
	v_pk_fma_f32 v[74:75], v[12:13], v[84:85], v[74:75]
	v_pk_fma_f32 v[68:69], v[14:15], v[80:81], v[68:69]
	v_pk_mul_f32 v[80:81], v[82:83], v[86:87] op_sel_hi:[0,1]
	v_pk_mul_f32 v[84:85], v[82:83], v[102:103] op_sel_hi:[0,1]
	s_waitcnt vmcnt(16)
	v_cvt_pk_f32_fp8_sdwa v[86:87], v109 src0_sel:WORD_1
	v_cvt_pk_f32_fp8_e32 v[102:103], v109
	v_pk_fma_f32 v[66:67], v[26:27], v[80:81], v[66:67]
	v_pk_fma_f32 v[76:77], v[24:25], v[84:85], v[76:77]
	v_pk_mul_f32 v[80:81], v[82:83], v[86:87] op_sel_hi:[0,1]
	v_pk_mul_f32 v[82:83], v[82:83], v[102:103] op_sel_hi:[0,1]
	v_pk_fma_f32 v[78:79], v[28:29], v[82:83], v[78:79]
	s_waitcnt vmcnt(15)
	v_cvt_pk_f32_fp8_e32 v[82:83], v108
	v_cvt_pk_f32_fp8_sdwa v[84:85], v108 src0_sel:WORD_1
	s_waitcnt vmcnt(14)
	v_cvt_pk_f32_fp8_e32 v[86:87], v107
	v_cvt_pk_f32_fp8_sdwa v[102:103], v107 src0_sel:WORD_1
	v_pk_fma_f32 v[64:65], v[30:31], v[80:81], v[64:65]
	v_mul_f32_e32 v80, 0x3d000000, v101
	v_pk_mul_f32 v[82:83], v[80:81], v[82:83] op_sel_hi:[0,1]
	v_pk_mul_f32 v[84:85], v[80:81], v[84:85] op_sel_hi:[0,1]
	v_pk_fma_f32 v[70:71], v[2:3], v[84:85], v[70:71]
	v_pk_fma_f32 v[72:73], v[0:1], v[82:83], v[72:73]
	v_pk_mul_f32 v[82:83], v[80:81], v[86:87] op_sel_hi:[0,1]
	v_pk_mul_f32 v[84:85], v[80:81], v[102:103] op_sel_hi:[0,1]
	s_waitcnt vmcnt(13)
	v_cvt_pk_f32_fp8_e32 v[86:87], v106
	v_cvt_pk_f32_fp8_sdwa v[102:103], v106 src0_sel:WORD_1
	v_pk_fma_f32 v[68:69], v[14:15], v[84:85], v[68:69]
	v_pk_fma_f32 v[74:75], v[12:13], v[82:83], v[74:75]
	v_pk_mul_f32 v[82:83], v[80:81], v[86:87] op_sel_hi:[0,1]
	v_pk_mul_f32 v[84:85], v[80:81], v[102:103] op_sel_hi:[0,1]
	s_waitcnt vmcnt(12)
	v_cvt_pk_f32_fp8_e32 v[86:87], v105
	v_cvt_pk_f32_fp8_sdwa v[102:103], v105 src0_sel:WORD_1
	v_pk_fma_f32 v[76:77], v[24:25], v[82:83], v[76:77]
	v_pk_fma_f32 v[66:67], v[26:27], v[84:85], v[66:67]
	v_pk_mul_f32 v[82:83], v[80:81], v[86:87] op_sel_hi:[0,1]
	v_pk_mul_f32 v[80:81], v[80:81], v[102:103] op_sel_hi:[0,1]
	v_pk_fma_f32 v[64:65], v[30:31], v[80:81], v[64:65]
	v_and_b32_sdwa v80, v73, v99 dst_sel:DWORD dst_unused:UNUSED_PAD src0_sel:WORD_1 src1_sel:DWORD
	v_and_b32_sdwa v81, v72, v99 dst_sel:DWORD dst_unused:UNUSED_PAD src0_sel:WORD_1 src1_sel:DWORD
	v_add3_u32 v73, v73, v80, s46
	v_and_b32_sdwa v80, v71, v99 dst_sel:DWORD dst_unused:UNUSED_PAD src0_sel:WORD_1 src1_sel:DWORD
	v_pk_fma_f32 v[78:79], v[28:29], v[82:83], v[78:79]
	v_add3_u32 v82, v72, v81, s46
	v_and_b32_sdwa v81, v70, v99 dst_sel:DWORD dst_unused:UNUSED_PAD src0_sel:WORD_1 src1_sel:DWORD
	v_add3_u32 v71, v71, v80, s46
	v_and_b32_sdwa v80, v75, v99 dst_sel:DWORD dst_unused:UNUSED_PAD src0_sel:WORD_1 src1_sel:DWORD
	v_add3_u32 v83, v70, v81, s46
	v_and_b32_sdwa v81, v74, v99 dst_sel:DWORD dst_unused:UNUSED_PAD src0_sel:WORD_1 src1_sel:DWORD
	v_add3_u32 v75, v75, v80, s46
	v_and_b32_sdwa v80, v69, v99 dst_sel:DWORD dst_unused:UNUSED_PAD src0_sel:WORD_1 src1_sel:DWORD
	v_add3_u32 v84, v74, v81, s46
	v_and_b32_sdwa v81, v68, v99 dst_sel:DWORD dst_unused:UNUSED_PAD src0_sel:WORD_1 src1_sel:DWORD
	v_add3_u32 v69, v69, v80, s46
	v_and_b32_sdwa v80, v77, v99 dst_sel:DWORD dst_unused:UNUSED_PAD src0_sel:WORD_1 src1_sel:DWORD
	v_add3_u32 v85, v68, v81, s46
	v_and_b32_sdwa v81, v76, v99 dst_sel:DWORD dst_unused:UNUSED_PAD src0_sel:WORD_1 src1_sel:DWORD
	v_add3_u32 v77, v77, v80, s46
	v_and_b32_sdwa v80, v67, v99 dst_sel:DWORD dst_unused:UNUSED_PAD src0_sel:WORD_1 src1_sel:DWORD
	v_add3_u32 v86, v76, v81, s46
	v_and_b32_sdwa v81, v66, v99 dst_sel:DWORD dst_unused:UNUSED_PAD src0_sel:WORD_1 src1_sel:DWORD
	v_add3_u32 v67, v67, v80, s46
	v_and_b32_sdwa v80, v79, v99 dst_sel:DWORD dst_unused:UNUSED_PAD src0_sel:WORD_1 src1_sel:DWORD
	v_add3_u32 v87, v66, v81, s46
	v_and_b32_sdwa v81, v78, v99 dst_sel:DWORD dst_unused:UNUSED_PAD src0_sel:WORD_1 src1_sel:DWORD
	v_add3_u32 v79, v79, v80, s46
	v_and_b32_sdwa v80, v65, v99 dst_sel:DWORD dst_unused:UNUSED_PAD src0_sel:WORD_1 src1_sel:DWORD
	v_and_b32_e32 v73, 0xffff0000, v73
	v_and_b32_e32 v72, 0xffff0000, v82
	v_add3_u32 v101, v78, v81, s46
	v_and_b32_sdwa v81, v64, v99 dst_sel:DWORD dst_unused:UNUSED_PAD src0_sel:WORD_1 src1_sel:DWORD
	v_add3_u32 v65, v65, v80, s46
	v_and_b32_e32 v71, 0xffff0000, v71
	v_and_b32_e32 v70, 0xffff0000, v83
	v_add3_u32 v102, v64, v81, s46
	v_and_b32_e32 v81, 0xffff0000, v65
	v_pk_fma_f32 v[64:65], v[72:73], v[72:73], 0 op_sel_hi:[1,1,0]
	v_and_b32_e32 v75, 0xffff0000, v75
	v_and_b32_e32 v74, 0xffff0000, v84
	v_pk_fma_f32 v[64:65], v[70:71], v[70:71], v[64:65]
	v_and_b32_e32 v69, 0xffff0000, v69
	v_and_b32_e32 v68, 0xffff0000, v85
	v_pk_fma_f32 v[64:65], v[74:75], v[74:75], v[64:65]
	v_and_b32_e32 v77, 0xffff0000, v77
	v_and_b32_e32 v76, 0xffff0000, v86
	v_pk_fma_f32 v[64:65], v[68:69], v[68:69], v[64:65]
	v_and_b32_e32 v67, 0xffff0000, v67
	v_and_b32_e32 v66, 0xffff0000, v87
	v_pk_fma_f32 v[64:65], v[76:77], v[76:77], v[64:65]
	v_and_b32_e32 v79, 0xffff0000, v79
	v_and_b32_e32 v78, 0xffff0000, v101
	v_pk_fma_f32 v[64:65], v[66:67], v[66:67], v[64:65]
	v_and_b32_e32 v80, 0xffff0000, v102
	v_pk_fma_f32 v[64:65], v[78:79], v[78:79], v[64:65]
	s_lshl_b64 s[24:25], s[20:21], 10
	v_pk_fma_f32 v[64:65], v[80:81], v[80:81], v[64:65]
	s_nop 0
	v_add_f32_e32 v64, v64, v65
	s_waitcnt lgkmcnt(0)
	s_nop 1
	v_add_f32_dpp v64, v64, v64 quad_perm:[1,0,3,2] row_mask:0xf bank_mask:0xf
	s_waitcnt lgkmcnt(0)
	s_nop 1
	v_add_f32_dpp v64, v64, v64 quad_perm:[2,3,0,1] row_mask:0xf bank_mask:0xf
	s_waitcnt lgkmcnt(0)
	s_nop 1
	v_add_f32_dpp v64, v64, v64 row_half_mirror row_mask:0xf bank_mask:0xf
	s_waitcnt lgkmcnt(0)
	s_nop 1
	v_add_f32_dpp v103, v64, v64 row_mirror row_mask:0xf bank_mask:0xf
	v_or_b32_sdwa v64, v73, v82 dst_sel:DWORD dst_unused:UNUSED_PAD src0_sel:DWORD src1_sel:WORD_1
	v_or_b32_sdwa v65, v71, v83 dst_sel:DWORD dst_unused:UNUSED_PAD src0_sel:DWORD src1_sel:WORD_1
	global_store_dwordx2 v[62:63], v[64:65], off
	v_or_b32_sdwa v64, v75, v84 dst_sel:DWORD dst_unused:UNUSED_PAD src0_sel:DWORD src1_sel:WORD_1
	s_waitcnt lgkmcnt(0)
	v_mov_b32_e32 v82, v103
	v_mov_b32_e32 v104, v103
	s_nop 1
	v_permlane16_swap_b32_e32 v82, v104
	v_add_f32_e32 v82, v82, v104
	v_or_b32_sdwa v65, v69, v85 dst_sel:DWORD dst_unused:UNUSED_PAD src0_sel:DWORD src1_sel:WORD_1
	global_store_dwordx2 v[62:63], v[64:65], off offset:512
	s_waitcnt lgkmcnt(0)
	v_mov_b32_e32 v64, v82
	v_mov_b32_e32 v83, v82
	s_nop 1
	v_permlane32_swap_b32_e32 v64, v83
	v_add_f32_e32 v64, v64, v83
	v_fmamk_f32 v64, v64, 0x3a800000, v96
	v_mul_f32_e32 v65, 0x4f800000, v64
	v_cmp_gt_f32_e32 vcc, s47, v64
	s_nop 1
	v_cndmask_b32_e32 v82, v64, v65, vcc
	v_sqrt_f32_e32 v83, v82
	v_or_b32_sdwa v64, v77, v86 dst_sel:DWORD dst_unused:UNUSED_PAD src0_sel:DWORD src1_sel:WORD_1
	v_or_b32_sdwa v65, v67, v87 dst_sel:DWORD dst_unused:UNUSED_PAD src0_sel:DWORD src1_sel:WORD_1
	global_store_dwordx2 v[62:63], v[64:65], off offset:1024
	v_add_u32_e32 v64, -1, v83
	v_fma_f32 v65, -v64, v83, v82
	v_cmp_ge_f32_e64 s[10:11], 0, v65
	v_add_u32_e32 v65, 1, v83
	v_mov_b32_e32 v86, 0
	v_cndmask_b32_e64 v64, v83, v64, s[10:11]
	v_fma_f32 v83, -v65, v83, v82
	v_cmp_lt_f32_e64 s[10:11], 0, v83
	s_nop 1
	v_cndmask_b32_e64 v64, v64, v65, s[10:11]
	v_mul_f32_e32 v65, 0x37800000, v64
	v_cndmask_b32_e32 v64, v64, v65, vcc
	v_cmp_class_f32_e32 vcc, v82, v97
	v_or_b32_sdwa v65, v81, v102 dst_sel:DWORD dst_unused:UNUSED_PAD src0_sel:DWORD src1_sel:WORD_1
	s_nop 0
	v_cndmask_b32_e32 v82, v64, v82, vcc
	v_div_scale_f32 v83, s[10:11], v82, v82, 1.0
	v_rcp_f32_e32 v84, v83
	v_or_b32_sdwa v64, v79, v101 dst_sel:DWORD dst_unused:UNUSED_PAD src0_sel:DWORD src1_sel:WORD_1
	global_store_dwordx2 v[62:63], v[64:65], off offset:1536
	v_fma_f32 v62, -v83, v84, 1.0
	v_fmac_f32_e32 v84, v62, v84
	v_div_scale_f32 v62, vcc, 1.0, v82, 1.0
	v_mul_f32_e32 v63, v62, v84
	v_fma_f32 v64, -v83, v63, v62
	v_fmac_f32_e32 v63, v64, v84
	v_fma_f32 v62, -v83, v63, v62
	v_div_fmas_f32 v62, v62, v84, v63
	v_div_fixup_f32 v82, v62, v82, 1.0
	v_pk_mul_f32 v[64:65], v[82:83], v[72:73] op_sel_hi:[0,1]
	v_pk_mul_f32 v[62:63], v[82:83], v[70:71] op_sel_hi:[0,1]
	v_pk_fma_f32 v[70:71], v[48:49], v[64:65], v[4:5]
	v_pk_mul_f32 v[64:65], v[82:83], v[68:69] op_sel_hi:[0,1]
	v_pk_mul_f32 v[68:69], v[82:83], v[76:77] op_sel_hi:[0,1]
	v_pk_mul_f32 v[72:73], v[82:83], v[74:75] op_sel_hi:[0,1]
	v_pk_fma_f32 v[74:75], v[56:57], v[68:69], v[16:17]
	v_pk_mul_f32 v[68:69], v[82:83], v[80:81] op_sel_hi:[0,1]
	v_bfe_u32 v80, v70, 16, 1
	v_add3_u32 v80, v70, v80, s46
	v_bfe_u32 v81, v71, 16, 1
	v_pk_fma_f32 v[62:63], v[46:47], v[62:63], v[6:7]
	v_lshrrev_b32_e32 v80, 16, v80
	v_add3_u32 v81, v71, v81, s46
	v_and_or_b32 v80, v81, s44, v80
	v_bfe_u32 v81, v62, 16, 1
	v_pk_mul_f32 v[66:67], v[82:83], v[66:67] op_sel_hi:[0,1]
	v_pk_mul_f32 v[76:77], v[82:83], v[78:79] op_sel_hi:[0,1]
	v_add3_u32 v81, v62, v81, s46
	v_bfe_u32 v82, v63, 16, 1
	v_lshrrev_b32_e32 v81, 16, v81
	v_add3_u32 v82, v63, v82, s46
	v_pk_fma_f32 v[72:73], v[52:53], v[72:73], v[8:9]
	v_lshl_add_u64 v[78:79], v[38:39], 0, s[22:23]
	v_and_or_b32 v81, v82, s44, v81
	global_store_dwordx2 v[78:79], v[80:81], off
	v_bfe_u32 v80, v72, 16, 1
	v_add3_u32 v80, v72, v80, s46
	v_bfe_u32 v81, v73, 16, 1
	v_pk_fma_f32 v[64:65], v[50:51], v[64:65], v[10:11]
	v_lshrrev_b32_e32 v80, 16, v80
	v_add3_u32 v81, v73, v81, s46
	v_and_or_b32 v80, v81, s44, v80
	v_bfe_u32 v81, v64, 16, 1
	v_add3_u32 v81, v64, v81, s46
	v_bfe_u32 v82, v65, 16, 1
	v_lshrrev_b32_e32 v81, 16, v81
	v_add3_u32 v82, v65, v82, s46
	v_and_or_b32 v81, v82, s44, v81
	global_store_dwordx2 v[78:79], v[80:81], off offset:512
	v_bfe_u32 v80, v74, 16, 1
	v_add3_u32 v80, v74, v80, s46
	v_bfe_u32 v81, v75, 16, 1
	v_pk_fma_f32 v[66:67], v[54:55], v[66:67], v[18:19]
	v_lshrrev_b32_e32 v80, 16, v80
	v_add3_u32 v81, v75, v81, s46
	v_and_or_b32 v80, v81, s44, v80
	v_bfe_u32 v81, v66, 16, 1
	v_add3_u32 v81, v66, v81, s46
	v_bfe_u32 v82, v67, 16, 1
	v_lshrrev_b32_e32 v81, 16, v81
	v_add3_u32 v82, v67, v82, s46
	v_pk_fma_f32 v[76:77], v[60:61], v[76:77], v[20:21]
	v_and_or_b32 v81, v82, s44, v81
	global_store_dwordx2 v[78:79], v[80:81], off offset:1024
	v_bfe_u32 v80, v76, 16, 1
	v_add3_u32 v80, v76, v80, s46
	v_bfe_u32 v81, v77, 16, 1
	v_pk_fma_f32 v[68:69], v[58:59], v[68:69], v[22:23]
	v_lshrrev_b32_e32 v80, 16, v80
	v_add3_u32 v81, v77, v81, s46
	v_mul_f32_e32 v83, 0x41000000, v70
	v_mul_f32_e32 v84, 0x41000000, v71
	v_and_or_b32 v80, v81, s44, v80
	v_bfe_u32 v81, v68, 16, 1
	v_med3_f32 v83, v83, s48, v100
	v_med3_f32 v84, v84, s48, v100
	v_add3_u32 v81, v68, v81, s46
	v_bfe_u32 v82, v69, 16, 1
	v_cvt_pk_fp8_f32 v86, v83, v84
	v_lshrrev_b32_e32 v81, 16, v81
	v_add3_u32 v82, v69, v82, s46
	v_mul_f32_e32 v85, 0x41000000, v62
	v_mul_f32_e32 v83, 0x41000000, v63
	v_and_or_b32 v81, v82, s44, v81
	v_med3_f32 v84, v85, s48, v100
	v_med3_f32 v83, v83, s48, v100
	global_store_dwordx2 v[78:79], v[80:81], off offset:1536
	v_mul_f32_e32 v78, 0x41000000, v72
	v_mul_f32_e32 v79, 0x41000000, v73
	v_cvt_pk_fp8_f32 v86, v84, v83 op_sel:[0,0,1]
	v_med3_f32 v78, v78, s48, v100
	v_med3_f32 v79, v79, s48, v100
	v_mov_b32_e32 v84, 0
	v_cvt_pk_fp8_f32 v84, v78, v79
	v_mul_f32_e32 v80, 0x41000000, v64
	v_mul_f32_e32 v78, 0x41000000, v65
	v_med3_f32 v79, v80, s48, v100
	v_med3_f32 v78, v78, s48, v100
	v_cvt_pk_fp8_f32 v84, v79, v78 op_sel:[0,0,1]
	v_mul_f32_e32 v78, 0x41000000, v74
	v_mul_f32_e32 v79, 0x41000000, v75
	v_med3_f32 v78, v78, s48, v100
	v_med3_f32 v79, v79, s48, v100
	v_mov_b32_e32 v85, 0
	v_cvt_pk_fp8_f32 v85, v78, v79
	v_mul_f32_e32 v80, 0x41000000, v66
	v_mul_f32_e32 v78, 0x41000000, v67
	v_med3_f32 v79, v80, s48, v100
	v_med3_f32 v78, v78, s48, v100
	v_lshl_add_u64 v[82:83], v[40:41], 0, s[24:25]
	v_cvt_pk_fp8_f32 v85, v79, v78 op_sel:[0,0,1]
	v_mul_f32_e32 v78, 0x41000000, v76
	v_mul_f32_e32 v79, 0x41000000, v77
	global_store_dword v[82:83], v86, off
	v_med3_f32 v78, v78, s48, v100
	v_med3_f32 v79, v79, s48, v100
	v_mov_b32_e32 v86, 0
	v_cvt_pk_fp8_f32 v86, v78, v79
	v_mul_f32_e32 v80, 0x41000000, v68
	v_mul_f32_e32 v78, 0x41000000, v69
	v_med3_f32 v79, v80, s48, v100
	v_med3_f32 v78, v78, s48, v100
	v_cvt_pk_fp8_f32 v86, v79, v78 op_sel:[0,0,1]
	ds_read_b128 v[78:81], v94
	global_store_dword v[82:83], v84, off offset:256
	global_store_dword v[82:83], v85, off offset:512
	global_store_dword v[82:83], v86, off offset:768
	ds_read_b128 v[82:85], v94 offset:1024
	ds_read_b128 v[102:105], v94 offset:2048
	s_waitcnt lgkmcnt(2)
	v_pk_fma_f32 v[78:79], v[70:71], v[78:79], 0 op_sel_hi:[1,1,0]
	s_nop 0
	v_pk_fma_f32 v[86:87], v[62:63], v[80:81], v[78:79]
	ds_read_b128 v[78:81], v94 offset:3072
	s_waitcnt lgkmcnt(2)
	v_pk_fma_f32 v[82:83], v[72:73], v[82:83], v[86:87]
	s_nop 0
	v_pk_fma_f32 v[82:83], v[64:65], v[84:85], v[82:83]
	s_waitcnt lgkmcnt(1)
	v_pk_fma_f32 v[82:83], v[74:75], v[102:103], v[82:83]
	s_nop 0
	v_pk_fma_f32 v[82:83], v[66:67], v[104:105], v[82:83]
	s_waitcnt lgkmcnt(0)
	v_pk_fma_f32 v[78:79], v[76:77], v[78:79], v[82:83]
	ds_read_b128 v[82:85], v94 offset:5120
	ds_read_b128 v[102:105], v94 offset:4096
	v_pk_fma_f32 v[78:79], v[68:69], v[80:81], v[78:79]
	s_waitcnt lgkmcnt(0)
	v_pk_fma_f32 v[86:87], v[70:71], v[102:103], 0 op_sel_hi:[1,1,0]
	v_add_f32_e32 v101, v78, v79
	ds_read_b128 v[78:81], v94 offset:7168
	ds_read_b128 v[106:109], v94 offset:6144
	v_pk_fma_f32 v[86:87], v[62:63], v[104:105], v[86:87]
	s_nop 0
	v_pk_fma_f32 v[82:83], v[72:73], v[82:83], v[86:87]
	s_nop 0
	v_pk_fma_f32 v[82:83], v[64:65], v[84:85], v[82:83]
	s_waitcnt lgkmcnt(0)
	v_pk_fma_f32 v[82:83], v[74:75], v[106:107], v[82:83]
	s_nop 0
	v_pk_fma_f32 v[82:83], v[66:67], v[108:109], v[82:83]
	s_nop 0
	v_pk_fma_f32 v[78:79], v[76:77], v[78:79], v[82:83]
	s_nop 0
	v_pk_fma_f32 v[78:79], v[68:69], v[80:81], v[78:79]
	s_nop 0
	v_add_f32_e32 v110, v78, v79
	ds_read_b128 v[78:81], v94 offset:8192
	ds_read_b128 v[82:85], v94 offset:9216
	ds_read_b128 v[102:105], v94 offset:10240
	ds_read_b128 v[106:109], v94 offset:11264
	s_waitcnt lgkmcnt(3)
	v_pk_fma_f32 v[78:79], v[70:71], v[78:79], 0 op_sel_hi:[1,1,0]
	s_nop 0
	v_pk_fma_f32 v[78:79], v[62:63], v[80:81], v[78:79]
	s_waitcnt lgkmcnt(2)
	v_pk_fma_f32 v[78:79], v[72:73], v[82:83], v[78:79]
	s_nop 0
	v_pk_fma_f32 v[78:79], v[64:65], v[84:85], v[78:79]
	s_waitcnt lgkmcnt(1)
	v_pk_fma_f32 v[78:79], v[74:75], v[102:103], v[78:79]
	s_nop 0
	v_pk_fma_f32 v[78:79], v[66:67], v[104:105], v[78:79]
	s_waitcnt lgkmcnt(0)
	v_pk_fma_f32 v[86:87], v[76:77], v[106:107], v[78:79]
	ds_read_b128 v[78:81], v94 offset:13312
	ds_read_b128 v[82:85], v94 offset:12288
	v_pk_fma_f32 v[86:87], v[68:69], v[108:109], v[86:87]
	ds_read_b128 v[102:105], v94 offset:15360
	ds_read_b128 v[106:109], v94 offset:14336
	v_add_f32_e32 v111, v86, v87
	s_waitcnt lgkmcnt(2)
	v_pk_fma_f32 v[82:83], v[70:71], v[82:83], 0 op_sel_hi:[1,1,0]
	s_nop 0
	v_pk_fma_f32 v[82:83], v[62:63], v[84:85], v[82:83]
	s_nop 0
	v_pk_fma_f32 v[78:79], v[72:73], v[78:79], v[82:83]
	s_nop 0
	v_pk_fma_f32 v[78:79], v[64:65], v[80:81], v[78:79]
	s_waitcnt lgkmcnt(0)
	v_pk_fma_f32 v[78:79], v[74:75], v[106:107], v[78:79]
	s_nop 0
	v_pk_fma_f32 v[78:79], v[66:67], v[108:109], v[78:79]
	s_nop 0
	v_pk_fma_f32 v[78:79], v[76:77], v[102:103], v[78:79]
	s_nop 0
	v_pk_fma_f32 v[78:79], v[68:69], v[104:105], v[78:79]
	s_nop 0
	v_add_f32_e32 v112, v78, v79
	ds_read_b128 v[78:81], v94 offset:16384
	ds_read_b128 v[82:85], v94 offset:17408
	ds_read_b128 v[102:105], v94 offset:18432
	ds_read_b128 v[106:109], v94 offset:19456
	s_waitcnt lgkmcnt(3)
	v_pk_fma_f32 v[78:79], v[70:71], v[78:79], 0 op_sel_hi:[1,1,0]
	s_nop 0
	v_pk_fma_f32 v[78:79], v[62:63], v[80:81], v[78:79]
	s_waitcnt lgkmcnt(2)
	v_pk_fma_f32 v[78:79], v[72:73], v[82:83], v[78:79]
	s_nop 0
	v_pk_fma_f32 v[78:79], v[64:65], v[84:85], v[78:79]
	s_waitcnt lgkmcnt(1)
	v_pk_fma_f32 v[78:79], v[74:75], v[102:103], v[78:79]
	s_nop 0
	v_pk_fma_f32 v[78:79], v[66:67], v[104:105], v[78:79]
	s_waitcnt lgkmcnt(0)
	v_pk_fma_f32 v[86:87], v[76:77], v[106:107], v[78:79]
	ds_read_b128 v[78:81], v94 offset:21504
	ds_read_b128 v[82:85], v94 offset:20480
	v_pk_fma_f32 v[86:87], v[68:69], v[108:109], v[86:87]
	ds_read_b128 v[102:105], v94 offset:23552
	ds_read_b128 v[106:109], v94 offset:22528
	v_add_f32_e32 v113, v86, v87
	s_waitcnt lgkmcnt(2)
	v_pk_fma_f32 v[82:83], v[70:71], v[82:83], 0 op_sel_hi:[1,1,0]
	s_nop 0
	v_pk_fma_f32 v[82:83], v[62:63], v[84:85], v[82:83]
	s_nop 0
	v_pk_fma_f32 v[78:79], v[72:73], v[78:79], v[82:83]
	s_nop 0
	v_pk_fma_f32 v[78:79], v[64:65], v[80:81], v[78:79]
	s_waitcnt lgkmcnt(0)
	v_pk_fma_f32 v[78:79], v[74:75], v[106:107], v[78:79]
	s_nop 0
	v_pk_fma_f32 v[78:79], v[66:67], v[108:109], v[78:79]
	s_nop 0
	v_pk_fma_f32 v[78:79], v[76:77], v[102:103], v[78:79]
	s_nop 0
	v_pk_fma_f32 v[78:79], v[68:69], v[104:105], v[78:79]
	s_nop 0
	v_add_f32_e32 v114, v78, v79
	ds_read_b128 v[78:81], v94 offset:24576
	ds_read_b128 v[82:85], v94 offset:25600
	ds_read_b128 v[102:105], v94 offset:26624
	ds_read_b128 v[106:109], v94 offset:27648
	s_waitcnt lgkmcnt(3)
	v_pk_fma_f32 v[78:79], v[70:71], v[78:79], 0 op_sel_hi:[1,1,0]
	s_nop 0
	v_pk_fma_f32 v[78:79], v[62:63], v[80:81], v[78:79]
	s_waitcnt lgkmcnt(2)
	v_pk_fma_f32 v[78:79], v[72:73], v[82:83], v[78:79]
	s_nop 0
	v_pk_fma_f32 v[78:79], v[64:65], v[84:85], v[78:79]
	s_waitcnt lgkmcnt(1)
	v_pk_fma_f32 v[78:79], v[74:75], v[102:103], v[78:79]
	s_nop 0
	v_pk_fma_f32 v[78:79], v[66:67], v[104:105], v[78:79]
	s_waitcnt lgkmcnt(0)
	v_pk_fma_f32 v[86:87], v[76:77], v[106:107], v[78:79]
	ds_read_b128 v[78:81], v94 offset:29696
	ds_read_b128 v[82:85], v94 offset:28672
	v_pk_fma_f32 v[86:87], v[68:69], v[108:109], v[86:87]
	ds_read_b128 v[102:105], v94 offset:31744
	ds_read_b128 v[106:109], v94 offset:30720
	v_add_f32_e32 v86, v86, v87
	s_waitcnt lgkmcnt(2)
	v_pk_fma_f32 v[70:71], v[70:71], v[82:83], 0 op_sel_hi:[1,1,0]
	s_nop 0
	v_pk_fma_f32 v[62:63], v[62:63], v[84:85], v[70:71]
	s_nop 0
	v_pk_fma_f32 v[62:63], v[72:73], v[78:79], v[62:63]
	s_nop 0
	v_pk_fma_f32 v[62:63], v[64:65], v[80:81], v[62:63]
	s_waitcnt lgkmcnt(0)
	v_pk_fma_f32 v[62:63], v[74:75], v[106:107], v[62:63]
	s_nop 0
	v_pk_fma_f32 v[62:63], v[66:67], v[108:109], v[62:63]
	s_nop 0
	v_pk_fma_f32 v[62:63], v[76:77], v[102:103], v[62:63]
	s_nop 0
	v_pk_fma_f32 v[62:63], v[68:69], v[104:105], v[62:63]
	s_nop 0
	v_add_f32_e32 v62, v62, v63
	s_waitcnt lgkmcnt(0)
	s_nop 1
	v_permlane32_swap_b32_e32 v101, v113
	v_add_f32_e32 v63, v101, v113
	s_waitcnt lgkmcnt(0)
	s_nop 1
	v_permlane32_swap_b32_e32 v110, v114
	v_add_f32_e32 v65, v110, v114
	s_waitcnt lgkmcnt(0)
	s_nop 1
	v_permlane32_swap_b32_e32 v111, v86
	v_add_f32_e32 v64, v111, v86
	s_waitcnt lgkmcnt(0)
	s_nop 1
	v_permlane32_swap_b32_e32 v112, v62
	v_add_f32_e32 v62, v112, v62
	s_waitcnt lgkmcnt(0)
	s_nop 1
	v_permlane16_swap_b32_e32 v63, v64
	v_add_f32_e32 v63, v63, v64
	s_waitcnt lgkmcnt(0)
	s_nop 1
	v_permlane16_swap_b32_e32 v65, v62
	v_add_f32_e32 v62, v65, v62
	v_cndmask_b32_e64 v64, v63, v62, s[6:7]
	s_nop 1
	v_mov_b32_dpp v64, v64 row_ror:8 row_mask:0xf bank_mask:0xf
	v_cndmask_b32_e64 v62, v62, v63, s[6:7]
	s_waitcnt lgkmcnt(0)
	v_add_f32_e32 v62, v62, v64
	s_nop 1
	v_mov_b32_dpp v63, v62 quad_perm:[3,2,1,0] row_mask:0xf bank_mask:0xf
	s_nop 1
	v_mov_b32_dpp v63, v63 row_half_mirror row_mask:0xf bank_mask:0xf
	s_waitcnt lgkmcnt(0)
	v_add_f32_e32 v62, v62, v63
	s_nop 1
	v_mov_b32_dpp v63, v62 quad_perm:[2,3,0,1] row_mask:0xf bank_mask:0xf
	s_waitcnt lgkmcnt(0)
	v_add_f32_e32 v62, v62, v63
	s_nop 1
	v_mov_b32_dpp v63, v62 quad_perm:[1,0,3,2] row_mask:0xf bank_mask:0xf
	s_and_saveexec_b64 s[10:11], s[8:9]
	s_cbranch_execz .LBB0_747
	s_lshl_b64 s[20:21], s[20:21], 5
	v_lshl_add_u64 v[64:65], v[42:43], 0, s[20:21]
	s_waitcnt lgkmcnt(0)
	v_add_f32_e32 v62, v62, v63
	global_store_dword v[64:65], v62, off
	s_branch .LBB0_747
